# v27 + thin passes: c/sqrtf(x) IEEE sqrt+divide sequences replaced by v_rsq_f32 (f32, 1 ulp)
# baseline (speedup 1.0000x reference)
; __device__ __forceinline__ void thin_pass(const Ctx& C, const bf16* hin, bf16* hout, bf16* u, float* out, const bf16* y, const float* gpost, float cmul, const float* gpre, bool last) {
;     ...
;         for (int b = 0; b < RB; ++b) { const v4u* yp = (const v4u*)(y + (size_t)(m0 + b) * D); const v4u* hp = (const v4u*)(hin + (size_t)(m0 + b) * D);
;             yr[b][0] = yp[lane]; yr[b][1] = yp[64 + lane]; hr[b][0] = hp[lane]; hr[b][1] = hp[64 + lane]; }
; #pragma unroll
;         for (int b = 0; b < RB; ++b) {
;             const int m = m0 + b; const v4u y0 = yr[b][0], y1 = yr[b][1], h0 = hr[b][0], h1 = hr[b][1];
;             f32x4 yv[4], h[4];
;             yv[0] = (f32x4){bf_lo(y0.x), bf_hi(y0.x), bf_lo(y0.y), bf_hi(y0.y)}; yv[1] = (f32x4){bf_lo(y0.z), bf_hi(y0.z), bf_lo(y0.w), bf_hi(y0.w)};
;             yv[2] = (f32x4){bf_lo(y1.x), bf_hi(y1.x), bf_lo(y1.y), bf_hi(y1.y)}; yv[3] = (f32x4){bf_lo(y1.z), bf_hi(y1.z), bf_lo(y1.w), bf_hi(y1.w)};
;             h[0] = (f32x4){bf_lo(h0.x), bf_hi(h0.x), bf_lo(h0.y), bf_hi(h0.y)}; h[1] = (f32x4){bf_lo(h0.z), bf_hi(h0.z), bf_lo(h0.w), bf_hi(h0.w)};
;             h[2] = (f32x4){bf_lo(h1.x), bf_hi(h1.x), bf_lo(h1.y), bf_hi(h1.y)}; h[3] = (f32x4){bf_lo(h1.z), bf_hi(h1.z), bf_lo(h1.w), bf_hi(h1.w)};
;             float ss = 0.f;
; #pragma unroll
;             for (int i = 0; i < 4; ++i) ss += (yv[i][0] * yv[i][0] + yv[i][1] * yv[i][1]) + (yv[i][2] * yv[i][2] + yv[i][3] * yv[i][3]);
;             const float ry = cmul / sqrtf(wave_sum(ss) * (1.0f / D) + RMS_EPS);
; #pragma unroll
;             for (int i = 0; i < 4; ++i) h[i] = h[i] + yv[i] * ry * g4[i];
.LBB0_734:
	v_lshl_add_u64 v[114:115], s[14:15], 0, v[100:101]
	v_add_co_u32_e32 v38, vcc, 0xd000000, v114
	v_lshl_add_u64 v[36:37], s[20:21], 0, v[100:101]
	s_nop 0
	v_addc_co_u32_e32 v39, vcc, 0, v115, vcc
	flat_load_dwordx4 v[84:87], v[36:37]
	flat_load_dwordx4 v[88:91], v[36:37] offset:1024
	flat_load_dwordx4 v[92:95], v[38:39] offset:1024
	flat_load_dwordx4 v[96:99], v[38:39]
	s_add_i32 s22, s10, 3
	flat_load_dwordx4 v[80:83], v[36:37] offset:2048
	flat_load_dwordx4 v[68:71], v[36:37] offset:3072
	v_add_co_u32_e32 v36, vcc, s84, v36
	s_ashr_i32 s23, s22, 31
	s_nop 0
	v_addc_co_u32_e32 v37, vcc, 0, v37, vcc
	v_add_co_u32_e32 v56, vcc, s91, v114
	s_lshl_b64 s[2:3], s[22:23], 11
	flat_load_dwordx4 v[64:67], v[36:37]
	flat_load_dwordx4 v[52:55], v[36:37] offset:1024
	v_lshl_add_u64 v[36:37], v[102:103], 0, s[2:3]
	v_lshl_add_u64 v[58:59], v[104:105], 0, s[2:3]
	v_addc_co_u32_e32 v57, vcc, 0, v115, vcc
	flat_load_dwordx4 v[76:79], v[38:39] offset:2048
	flat_load_dwordx4 v[72:75], v[38:39] offset:3072
	flat_load_dwordx4 v[44:47], v[36:37]
	flat_load_dwordx4 v[40:43], v[36:37] offset:1024
	flat_load_dwordx4 v[48:51], v[58:59]
	s_nop 0
	flat_load_dwordx4 v[36:39], v[58:59] offset:1024
	flat_load_dwordx4 v[60:63], v[56:57]
	s_nop 0
	flat_load_dwordx4 v[56:59], v[56:57] offset:1024
	s_waitcnt vmcnt(0) lgkmcnt(0)
	v_lshlrev_b32_e32 v118, 16, v86
	v_and_b32_e32 v119, 0xffff0000, v86
	v_lshlrev_b32_e32 v124, 16, v94
	v_and_b32_e32 v142, 0xffff0000, v94
	v_lshlrev_b32_e32 v86, 16, v96
	v_lshlrev_b32_e32 v94, 16, v97
	v_lshlrev_b32_e32 v120, 16, v87
	v_and_b32_e32 v121, 0xffff0000, v87
	v_lshlrev_b32_e32 v122, 16, v88
	v_and_b32_e32 v123, 0xffff0000, v88
	v_lshlrev_b32_e32 v126, 16, v95
	v_and_b32_e32 v127, 0xffff0000, v95
	v_and_b32_e32 v87, 0xffff0000, v96
	v_and_b32_e32 v95, 0xffff0000, v97
	v_lshlrev_b32_e32 v97, 16, v99
	v_lshlrev_b32_e32 v96, 16, v98
	v_and_b32_e32 v99, 0xffff0000, v99
	v_and_b32_e32 v98, 0xffff0000, v98
	v_mul_f32_e32 v2, v86, v86
	v_mul_f32_e32 v88, v94, v94
	v_lshlrev_b32_e32 v128, 16, v92
	v_and_b32_e32 v129, 0xffff0000, v92
	v_lshlrev_b32_e32 v92, 16, v93
	v_pk_mul_f32 v[130:131], v[98:99], v[98:99]
	v_pk_fma_f32 v[138:139], v[86:87], v[86:87], v[2:3] op_sel_hi:[1,1,0]
	v_pk_fma_f32 v[140:141], v[94:95], v[94:95], v[88:89] op_sel_hi:[1,1,0]
	v_and_b32_e32 v93, 0xffff0000, v93
	v_mul_f32_e32 v132, v128, v128
	v_mul_f32_e32 v134, v92, v92
	v_mov_b32_e32 v136, v124
	v_pk_fma_f32 v[130:131], v[96:97], v[96:97], v[130:131]
	v_mov_b32_e32 v125, v139
	v_mov_b32_e32 v137, v141
	v_pk_fma_f32 v[132:133], v[128:129], v[128:129], v[132:133] op_sel_hi:[1,1,0]
	v_pk_fma_f32 v[134:135], v[92:93], v[92:93], v[134:135] op_sel_hi:[1,1,0]
	v_pk_add_f32 v[130:131], v[130:131], v[130:131] op_sel_hi:[0,1]
	v_pk_add_f32 v[138:139], v[138:139], v[140:141]
	v_pk_mul_f32 v[136:137], v[124:125], v[136:137]
	v_mul_f32_e32 v132, v126, v126
	v_mul_f32_e32 v134, v127, v127
	v_mul_f32_e32 v130, v142, v142
	v_mov_b32_e32 v137, v139
	v_pk_add_f32 v[132:133], v[132:133], v[134:135]
	v_pk_add_f32 v[130:131], v[136:137], v[130:131]
	v_lshlrev_b32_e32 v134, 16, v91
	v_pk_add_f32 v[130:131], v[130:131], v[132:133]
	v_lshlrev_b32_e32 v132, 16, v90
	v_add_f32_e32 v2, v130, v131
	v_and_b32_e32 v135, 0xffff0000, v91
	v_lshlrev_b32_e32 v116, 16, v84
	v_add_f32_dpp v2, v2, v2 quad_perm:[1,0,3,2] row_mask:0xf bank_mask:0xf bound_ctrl:1
	v_and_b32_e32 v117, 0xffff0000, v84
	v_lshlrev_b32_e32 v84, 16, v85
	v_add_f32_dpp v2, v2, v2 quad_perm:[2,3,0,1] row_mask:0xf bank_mask:0xf bound_ctrl:1
	v_and_b32_e32 v85, 0xffff0000, v85
	s_nop 0
	v_add_f32_dpp v2, v2, v2 row_half_mirror row_mask:0xf bank_mask:0xf bound_ctrl:1
	s_nop 1
	v_add_f32_dpp v2, v2, v2 row_mirror row_mask:0xf bank_mask:0xf bound_ctrl:1
	s_nop 0
	v_readlane_b32 s1, v2, 16
	v_readlane_b32 s4, v2, 48
	v_readlane_b32 s2, v2, 0
	v_readlane_b32 s3, v2, 32
	v_mov_b32_e32 v130, s1
	v_mov_b32_e32 v131, s4
	v_pk_add_f32 v[130:131], s[2:3], v[130:131]
	s_mov_b64 s[4:5], -1
	v_add_f32_e32 v2, v130, v131
	v_fmamk_f32 v2, v2, 0x3a800000, v214
	v_lshlrev_b32_e32 v130, 16, v89
	v_and_b32_e32 v131, 0xffff0000, v89
	v_and_b32_e32 v133, 0xffff0000, v90
	v_rsq_f32_e32 v2, v2
	s_nop 0
	v_mul_f32_e32 v2, 0.5, v2
	v_pk_mul_f32 v[88:89], v[2:3], v[86:87] op_sel_hi:[0,1]
	v_pk_mul_f32 v[86:87], v[2:3], v[94:95] op_sel_hi:[0,1]
	v_pk_fma_f32 v[86:87], v[10:11], v[86:87], v[84:85]
	v_pk_fma_f32 v[84:85], v[8:9], v[88:89], v[116:117]
	v_mov_b32_e32 v88, v96
	v_mov_b32_e32 v89, v98
	v_mov_b32_e32 v98, v97
	v_pk_mul_f32 v[96:97], v[2:3], v[128:129] op_sel_hi:[0,1]
	v_pk_mul_f32 v[92:93], v[2:3], v[92:93] op_sel_hi:[0,1]
	v_mov_b32_e32 v125, v142
	v_pk_mul_f32 v[88:89], v[2:3], v[88:89] op_sel_hi:[0,1]
	v_pk_mul_f32 v[90:91], v[2:3], v[98:99] op_sel_hi:[0,1]
	v_pk_fma_f32 v[94:95], v[18:19], v[92:93], v[130:131]
	v_pk_fma_f32 v[92:93], v[16:17], v[96:97], v[122:123]
	v_pk_mul_f32 v[96:97], v[124:125], v[2:3] op_sel_hi:[1,0]
	v_pk_mul_f32 v[98:99], v[126:127], v[2:3] op_sel_hi:[1,0]
	v_cndmask_b32_e64 v2, 0, 1, s[6:7]
	v_pk_fma_f32 v[90:91], v[6:7], v[90:91], v[120:121]
	v_pk_fma_f32 v[88:89], v[4:5], v[88:89], v[118:119]
	v_pk_fma_f32 v[98:99], v[14:15], v[98:99], v[134:135]
	v_pk_fma_f32 v[96:97], v[12:13], v[96:97], v[132:133]
	v_cmp_ne_u32_e64 s[2:3], 1, v2
	s_andn2_b64 vcc, exec, s[6:7]
	v_lshl_add_u64 v[116:117], s[18:19], 0, v[100:101]
	s_cbranch_vccnz .LBB0_736
; __device__ __forceinline__ unsigned pk2(float lo, float hi) { unsigned r; asm("v_cvt_pk_bf16_f32 %0, %1, %2" : "=v"(r) : "v"(lo), "v"(hi)); return r; }
; __device__ __forceinline__ void thin_pass(const Ctx& C, const bf16* hin, bf16* hout, bf16* u, float* out, const bf16* y, const float* gpost, float cmul, const float* gpre, bool last) {
;     ...
;                 float s2 = 0.f;
; #pragma unroll
;                 for (int i = 0; i < 4; ++i) s2 += (h[i][0] * h[i][0] + h[i][1] * h[i][1]) + (h[i][2] * h[i][2] + h[i][3] * h[i][3]);
;                 const float rh = 1.0f / sqrtf(wave_sum(s2) * (1.0f / D) + RMS_EPS);
;                 v4u o0, o1; o0.x = pk2(h[0][0], h[0][1]); o0.y = pk2(h[0][2], h[0][3]); o0.z = pk2(h[1][0], h[1][1]); o0.w = pk2(h[1][2], h[1][3]);
;                 o1.x = pk2(h[2][0], h[2][1]); o1.y = pk2(h[2][2], h[2][3]); o1.z = pk2(h[3][0], h[3][1]); o1.w = pk2(h[3][2], h[3][3]);
;                 v4u* hp = (v4u*)(hout + (size_t)m * D); hp[lane] = o0; hp[64 + lane] = o1;
; #pragma unroll
;                 for (int i = 0; i < 4; ++i) h[i] = h[i] * rh * q4[i];
;                 o0.x = pk2(h[0][0], h[0][1]); o0.y = pk2(h[0][2], h[0][3]); o0.z = pk2(h[1][0], h[1][1]); o0.w = pk2(h[1][2], h[1][3]);
;                 o1.x = pk2(h[2][0], h[2][1]); o1.y = pk2(h[2][2], h[2][3]); o1.z = pk2(h[3][0], h[3][1]); o1.w = pk2(h[3][2], h[3][3]);
;                 v4u* up = (v4u*)(u + (size_t)m * D); up[lane] = o0; up[64 + lane] = o1;
	v_pk_mul_f32 v[118:119], v[86:87], v[86:87]
	v_pk_mul_f32 v[120:121], v[84:85], v[84:85]
	v_mul_f32_e32 v2, v92, v92
	v_pk_mov_b32 v[122:123], v[120:121], v[118:119] op_sel:[1,0]
	v_mov_b32_e32 v121, v119
	v_pk_add_f32 v[118:119], v[122:123], v[120:121]
	v_pk_mul_f32 v[120:121], v[90:91], v[90:91]
	v_pk_mul_f32 v[122:123], v[88:89], v[88:89]
	v_pk_add_f32 v[118:119], v[118:119], v[118:119] op_sel_hi:[0,1]
	v_pk_mov_b32 v[124:125], v[122:123], v[120:121] op_sel:[1,0]
	v_mov_b32_e32 v123, v121
	v_pk_add_f32 v[120:121], v[124:125], v[122:123]
	v_pk_fma_f32 v[122:123], v[92:93], v[92:93], v[2:3] op_sel_hi:[1,1,0]
	v_mul_f32_e32 v2, v94, v94
	v_pk_add_f32 v[120:121], v[120:121], v[120:121] op_sel_hi:[0,1]
	v_pk_fma_f32 v[124:125], v[94:95], v[94:95], v[2:3] op_sel_hi:[1,1,0]
	v_mul_f32_e32 v122, v96, v96
	v_mul_f32_e32 v124, v97, v97
	v_mul_f32_e32 v118, v98, v98
	v_mul_f32_e32 v120, v99, v99
	v_pk_add_f32 v[122:123], v[122:123], v[124:125]
	v_pk_add_f32 v[118:119], v[118:119], v[120:121]
	v_cvt_pk_bf16_f32 v124, v96, v97
	v_cvt_pk_bf16_f32 v125, v98, v99
	s_nop 0
	v_pk_add_f32 v[118:119], v[122:123], v[118:119]
	v_cvt_pk_bf16_f32 v123, v94, v95
	s_nop 0
	v_add_f32_e32 v2, v118, v119
	s_nop 1
	v_add_f32_dpp v2, v2, v2 quad_perm:[1,0,3,2] row_mask:0xf bank_mask:0xf bound_ctrl:1
	s_nop 1
	v_add_f32_dpp v2, v2, v2 quad_perm:[2,3,0,1] row_mask:0xf bank_mask:0xf bound_ctrl:1
	s_nop 1
	v_add_f32_dpp v2, v2, v2 row_half_mirror row_mask:0xf bank_mask:0xf bound_ctrl:1
	s_nop 1
	v_add_f32_dpp v2, v2, v2 row_mirror row_mask:0xf bank_mask:0xf bound_ctrl:1
	s_nop 0
	v_readlane_b32 s1, v2, 16
	v_readlane_b32 s9, v2, 48
	v_readlane_b32 s4, v2, 0
	v_readlane_b32 s5, v2, 32
	v_mov_b32_e32 v118, s1
	v_mov_b32_e32 v119, s9
	v_pk_add_f32 v[118:119], s[4:5], v[118:119]
	s_brev_b32 s1, 64
	v_add_f32_e32 v2, v118, v119
	v_fmamk_f32 v2, v2, 0x3a800000, v214
	s_mov_b64 s[4:5], 0
	v_add_co_u32_e32 v126, vcc, s1, v116
	v_rsq_f32_e32 v2, v2
	s_nop 0
	v_cvt_pk_bf16_f32 v118, v84, v85
	v_cvt_pk_bf16_f32 v119, v86, v87
	v_cvt_pk_bf16_f32 v120, v88, v89
	v_cvt_pk_bf16_f32 v121, v90, v91
	v_cvt_pk_bf16_f32 v122, v92, v93
	s_nop 0
	v_addc_co_u32_e32 v127, vcc, 0, v117, vcc
	global_store_dwordx4 v[126:127], v[118:121], off
	global_store_dwordx4 v[126:127], v[122:125], off offset:1024
	v_pk_mul_f32 v[126:127], v[92:93], v[2:3] op_sel_hi:[1,0]
	v_pk_mul_f32 v[118:119], v[84:85], v[2:3] op_sel_hi:[1,0]
	v_pk_mul_f32 v[120:121], v[86:87], v[2:3] op_sel_hi:[1,0]
	v_pk_mul_f32 v[122:123], v[88:89], v[2:3] op_sel_hi:[1,0]
	v_pk_mul_f32 v[120:121], v[26:27], v[120:121]
	v_pk_mul_f32 v[118:119], v[24:25], v[118:119]
	v_pk_mul_f32 v[122:123], v[20:21], v[122:123]
	v_pk_mul_f32 v[126:127], v[32:33], v[126:127]
	v_pk_mul_f32 v[124:125], v[90:91], v[2:3] op_sel_hi:[1,0]
	v_cvt_pk_bf16_f32 v118, v118, v119
	v_cvt_pk_bf16_f32 v119, v120, v121
	v_cvt_pk_bf16_f32 v120, v122, v123
	v_cvt_pk_bf16_f32 v122, v126, v127
	v_add_co_u32_e32 v126, vcc, 0xb000000, v114
	v_pk_mul_f32 v[124:125], v[22:23], v[124:125]
	v_pk_mul_f32 v[128:129], v[94:95], v[2:3] op_sel_hi:[1,0]
	v_pk_mul_f32 v[130:131], v[96:97], v[2:3] op_sel_hi:[1,0]
	v_pk_mul_f32 v[132:133], v[98:99], v[2:3] op_sel_hi:[1,0]
	v_cvt_pk_bf16_f32 v121, v124, v125
	v_addc_co_u32_e32 v127, vcc, 0, v115, vcc
	v_pk_mul_f32 v[128:129], v[34:35], v[128:129]
	v_pk_mul_f32 v[132:133], v[30:31], v[132:133]
	v_pk_mul_f32 v[130:131], v[28:29], v[130:131]
	v_cvt_pk_bf16_f32 v123, v128, v129
	v_cvt_pk_bf16_f32 v125, v132, v133
	s_nop 0
	v_cvt_pk_bf16_f32 v124, v130, v131
	flat_store_dwordx4 v[126:127], v[118:121]
	flat_store_dwordx4 v[126:127], v[122:125] offset:1024

; __device__ __forceinline__ void thin_pass(const Ctx& C, const bf16* hin, bf16* hout, bf16* u, float* out, const bf16* y, const float* gpost, float cmul, const float* gpre, bool last) {
;     ...
;         for (int b = 0; b < RB; ++b) {
;             const int m = m0 + b; const v4u y0 = yr[b][0], y1 = yr[b][1], h0 = hr[b][0], h1 = hr[b][1];
;             f32x4 yv[4], h[4];
;             yv[0] = (f32x4){bf_lo(y0.x), bf_hi(y0.x), bf_lo(y0.y), bf_hi(y0.y)}; yv[1] = (f32x4){bf_lo(y0.z), bf_hi(y0.z), bf_lo(y0.w), bf_hi(y0.w)};
;             yv[2] = (f32x4){bf_lo(y1.x), bf_hi(y1.x), bf_lo(y1.y), bf_hi(y1.y)}; yv[3] = (f32x4){bf_lo(y1.z), bf_hi(y1.z), bf_lo(y1.w), bf_hi(y1.w)};
;             h[0] = (f32x4){bf_lo(h0.x), bf_hi(h0.x), bf_lo(h0.y), bf_hi(h0.y)}; h[1] = (f32x4){bf_lo(h0.z), bf_hi(h0.z), bf_lo(h0.w), bf_hi(h0.w)};
;             h[2] = (f32x4){bf_lo(h1.x), bf_hi(h1.x), bf_lo(h1.y), bf_hi(h1.y)}; h[3] = (f32x4){bf_lo(h1.z), bf_hi(h1.z), bf_lo(h1.w), bf_hi(h1.w)};
;             float ss = 0.f;
; #pragma unroll
;             for (int i = 0; i < 4; ++i) ss += (yv[i][0] * yv[i][0] + yv[i][1] * yv[i][1]) + (yv[i][2] * yv[i][2] + yv[i][3] * yv[i][3]);
;             const float ry = cmul / sqrtf(wave_sum(ss) * (1.0f / D) + RMS_EPS);
; #pragma unroll
;             for (int i = 0; i < 4; ++i) h[i] = h[i] + yv[i] * ry * g4[i];
.LBB0_738:
	s_nop 0
	v_lshlrev_b32_e32 v92, 16, v76
	v_and_b32_e32 v93, 0xffff0000, v76
	v_mul_f32_e32 v2, v92, v92
	v_lshlrev_b32_e32 v76, 16, v77
	v_pk_fma_f32 v[94:95], v[92:93], v[92:93], v[2:3] op_sel_hi:[1,1,0]
	v_and_b32_e32 v77, 0xffff0000, v77
	v_mul_f32_e32 v2, v76, v76
	v_lshlrev_b32_e32 v99, 16, v79
	v_lshlrev_b32_e32 v98, 16, v78
	v_and_b32_e32 v79, 0xffff0000, v79
	v_and_b32_e32 v78, 0xffff0000, v78
	v_lshlrev_b32_e32 v120, 16, v72
	v_lshlrev_b32_e32 v84, 16, v74
	v_pk_fma_f32 v[96:97], v[76:77], v[76:77], v[2:3] op_sel_hi:[1,1,0]
	v_pk_mul_f32 v[118:119], v[78:79], v[78:79]
	v_and_b32_e32 v121, 0xffff0000, v72
	v_mul_f32_e32 v2, v120, v120
	v_lshlrev_b32_e32 v124, 16, v73
	v_pk_fma_f32 v[118:119], v[98:99], v[98:99], v[118:119]
	v_pk_fma_f32 v[122:123], v[120:121], v[120:121], v[2:3] op_sel_hi:[1,1,0]
	v_and_b32_e32 v125, 0xffff0000, v73
	v_mul_f32_e32 v2, v124, v124
	v_mov_b32_e32 v85, v95
	v_mov_b32_e32 v126, v84
	v_mov_b32_e32 v127, v97
	v_and_b32_e32 v128, 0xffff0000, v74
	v_lshlrev_b32_e32 v86, 16, v75
	v_and_b32_e32 v87, 0xffff0000, v75
	v_pk_add_f32 v[118:119], v[118:119], v[118:119] op_sel_hi:[0,1]
	v_pk_fma_f32 v[72:73], v[124:125], v[124:125], v[2:3] op_sel_hi:[1,1,0]
	v_pk_mul_f32 v[126:127], v[84:85], v[126:127]
	v_pk_add_f32 v[94:95], v[94:95], v[96:97]
	v_mul_f32_e32 v118, v128, v128
	v_mul_f32_e32 v122, v86, v86
	v_mul_f32_e32 v72, v87, v87
	v_mov_b32_e32 v127, v95
	v_pk_add_f32 v[94:95], v[126:127], v[118:119]
	v_pk_add_f32 v[72:73], v[122:123], v[72:73]
	v_lshlrev_b32_e32 v90, 16, v68
	v_pk_add_f32 v[72:73], v[94:95], v[72:73]
	v_and_b32_e32 v91, 0xffff0000, v68
	v_add_f32_e32 v2, v72, v73
	v_lshlrev_b32_e32 v94, 16, v69
	v_and_b32_e32 v95, 0xffff0000, v69
	v_add_f32_dpp v2, v2, v2 quad_perm:[1,0,3,2] row_mask:0xf bank_mask:0xf bound_ctrl:1
	v_lshlrev_b32_e32 v96, 16, v70
	v_and_b32_e32 v97, 0xffff0000, v70
	v_add_f32_dpp v2, v2, v2 quad_perm:[2,3,0,1] row_mask:0xf bank_mask:0xf bound_ctrl:1
	v_lshlrev_b32_e32 v118, 16, v71
	v_and_b32_e32 v119, 0xffff0000, v71
	v_add_f32_dpp v2, v2, v2 row_half_mirror row_mask:0xf bank_mask:0xf bound_ctrl:1
	v_lshlrev_b32_e32 v74, 16, v80
	v_and_b32_e32 v75, 0xffff0000, v80
	v_add_f32_dpp v2, v2, v2 row_mirror row_mask:0xf bank_mask:0xf bound_ctrl:1
	v_lshlrev_b32_e32 v80, 16, v81
	v_readlane_b32 s1, v2, 16
	v_readlane_b32 s9, v2, 48
	v_readlane_b32 s4, v2, 0
	v_readlane_b32 s5, v2, 32
	v_mov_b32_e32 v72, s1
	v_mov_b32_e32 v73, s9
	v_pk_add_f32 v[72:73], s[4:5], v[72:73]
	v_and_b32_e32 v81, 0xffff0000, v81
	v_add_f32_e32 v2, v72, v73
	v_fmamk_f32 v2, v2, 0x3a800000, v214
	v_mov_b32_e32 v73, v78
	v_mov_b32_e32 v78, v99
	v_lshlrev_b32_e32 v88, 16, v82
	v_and_b32_e32 v89, 0xffff0000, v82
	v_lshlrev_b32_e32 v82, 16, v83
	v_and_b32_e32 v83, 0xffff0000, v83
	v_mov_b32_e32 v85, v128
	s_mov_b64 s[4:5], -1
	v_rsq_f32_e32 v2, v2
	s_nop 0
	v_mul_f32_e32 v2, 0.5, v2
	v_pk_mul_f32 v[68:69], v[2:3], v[92:93] op_sel_hi:[0,1]
	v_pk_mul_f32 v[70:71], v[2:3], v[76:77] op_sel_hi:[0,1]
	v_pk_fma_f32 v[68:69], v[8:9], v[68:69], v[74:75]
	v_mov_b32_e32 v72, v98
	v_pk_mul_f32 v[74:75], v[2:3], v[78:79] op_sel_hi:[0,1]
	v_pk_fma_f32 v[70:71], v[10:11], v[70:71], v[80:81]
	v_pk_mul_f32 v[72:73], v[2:3], v[72:73] op_sel_hi:[0,1]
	v_pk_fma_f32 v[74:75], v[6:7], v[74:75], v[82:83]
	v_pk_mul_f32 v[76:77], v[2:3], v[120:121] op_sel_hi:[0,1]
	v_pk_mul_f32 v[78:79], v[2:3], v[124:125] op_sel_hi:[0,1]
	v_pk_mul_f32 v[80:81], v[84:85], v[2:3] op_sel_hi:[1,0]
	v_pk_mul_f32 v[82:83], v[86:87], v[2:3] op_sel_hi:[1,0]
	v_pk_fma_f32 v[72:73], v[4:5], v[72:73], v[88:89]
	v_pk_fma_f32 v[78:79], v[18:19], v[78:79], v[94:95]
	v_pk_fma_f32 v[76:77], v[16:17], v[76:77], v[90:91]
	v_pk_fma_f32 v[82:83], v[14:15], v[82:83], v[118:119]
	v_pk_fma_f32 v[80:81], v[12:13], v[80:81], v[96:97]
	s_and_b64 vcc, exec, s[2:3]
	s_cbranch_vccnz .LBB0_740
; __device__ __forceinline__ unsigned pk2(float lo, float hi) { unsigned r; asm("v_cvt_pk_bf16_f32 %0, %1, %2" : "=v"(r) : "v"(lo), "v"(hi)); return r; }
; __device__ __forceinline__ void thin_pass(const Ctx& C, const bf16* hin, bf16* hout, bf16* u, float* out, const bf16* y, const float* gpost, float cmul, const float* gpre, bool last) {
;     ...
;                 float s2 = 0.f;
; #pragma unroll
;                 for (int i = 0; i < 4; ++i) s2 += (h[i][0] * h[i][0] + h[i][1] * h[i][1]) + (h[i][2] * h[i][2] + h[i][3] * h[i][3]);
;                 const float rh = 1.0f / sqrtf(wave_sum(s2) * (1.0f / D) + RMS_EPS);
;                 v4u o0, o1; o0.x = pk2(h[0][0], h[0][1]); o0.y = pk2(h[0][2], h[0][3]); o0.z = pk2(h[1][0], h[1][1]); o0.w = pk2(h[1][2], h[1][3]);
;                 o1.x = pk2(h[2][0], h[2][1]); o1.y = pk2(h[2][2], h[2][3]); o1.z = pk2(h[3][0], h[3][1]); o1.w = pk2(h[3][2], h[3][3]);
;                 v4u* hp = (v4u*)(hout + (size_t)m * D); hp[lane] = o0; hp[64 + lane] = o1;
; #pragma unroll
;                 for (int i = 0; i < 4; ++i) h[i] = h[i] * rh * q4[i];
;                 o0.x = pk2(h[0][0], h[0][1]); o0.y = pk2(h[0][2], h[0][3]); o0.z = pk2(h[1][0], h[1][1]); o0.w = pk2(h[1][2], h[1][3]);
;                 o1.x = pk2(h[2][0], h[2][1]); o1.y = pk2(h[2][2], h[2][3]); o1.z = pk2(h[3][0], h[3][1]); o1.w = pk2(h[3][2], h[3][3]);
;                 v4u* up = (v4u*)(u + (size_t)m * D); up[lane] = o0; up[64 + lane] = o1;
	v_pk_mul_f32 v[84:85], v[70:71], v[70:71]
	v_pk_mul_f32 v[86:87], v[68:69], v[68:69]
	v_mul_f32_e32 v2, v76, v76
	v_pk_mov_b32 v[88:89], v[86:87], v[84:85] op_sel:[1,0]
	v_mov_b32_e32 v87, v85
	v_pk_add_f32 v[84:85], v[88:89], v[86:87]
	v_pk_mul_f32 v[86:87], v[74:75], v[74:75]
	v_pk_mul_f32 v[88:89], v[72:73], v[72:73]
	v_pk_add_f32 v[84:85], v[84:85], v[84:85] op_sel_hi:[0,1]
	v_pk_mov_b32 v[90:91], v[88:89], v[86:87] op_sel:[1,0]
	v_mov_b32_e32 v89, v87
	v_pk_add_f32 v[86:87], v[90:91], v[88:89]
	v_pk_fma_f32 v[88:89], v[76:77], v[76:77], v[2:3] op_sel_hi:[1,1,0]
	v_mul_f32_e32 v2, v78, v78
	v_pk_add_f32 v[86:87], v[86:87], v[86:87] op_sel_hi:[0,1]
	v_pk_fma_f32 v[90:91], v[78:79], v[78:79], v[2:3] op_sel_hi:[1,1,0]
	v_mul_f32_e32 v88, v80, v80
	v_mul_f32_e32 v90, v81, v81
	v_mul_f32_e32 v84, v82, v82
	v_mul_f32_e32 v86, v83, v83
	v_pk_add_f32 v[88:89], v[88:89], v[90:91]
	v_pk_add_f32 v[84:85], v[84:85], v[86:87]
	v_cvt_pk_bf16_f32 v90, v80, v81
	v_cvt_pk_bf16_f32 v91, v82, v83
	s_nop 0
	v_pk_add_f32 v[84:85], v[88:89], v[84:85]
	v_cvt_pk_bf16_f32 v89, v78, v79
	s_nop 0
	v_add_f32_e32 v2, v84, v85
	s_nop 1
	v_add_f32_dpp v2, v2, v2 quad_perm:[1,0,3,2] row_mask:0xf bank_mask:0xf bound_ctrl:1
	s_nop 1
	v_add_f32_dpp v2, v2, v2 quad_perm:[2,3,0,1] row_mask:0xf bank_mask:0xf bound_ctrl:1
	s_nop 1
	v_add_f32_dpp v2, v2, v2 row_half_mirror row_mask:0xf bank_mask:0xf bound_ctrl:1
	s_nop 1
	v_add_f32_dpp v2, v2, v2 row_mirror row_mask:0xf bank_mask:0xf bound_ctrl:1
	s_nop 0
	v_readlane_b32 s1, v2, 16
	v_readlane_b32 s9, v2, 48
	v_readlane_b32 s4, v2, 0
	v_readlane_b32 s5, v2, 32
	v_mov_b32_e32 v84, s1
	v_mov_b32_e32 v85, s9
	v_pk_add_f32 v[84:85], s[4:5], v[84:85]
	s_brev_b32 s1, 64
	v_add_f32_e32 v2, v84, v85
	v_fmamk_f32 v2, v2, 0x3a800000, v214
	s_mov_b64 s[4:5], 0
	v_add_co_u32_e32 v92, vcc, s1, v116
	v_rsq_f32_e32 v2, v2
	s_nop 0
	v_cvt_pk_bf16_f32 v84, v68, v69
	v_cvt_pk_bf16_f32 v85, v70, v71
	v_cvt_pk_bf16_f32 v86, v72, v73
	v_cvt_pk_bf16_f32 v87, v74, v75
	v_cvt_pk_bf16_f32 v88, v76, v77
	s_nop 0
	v_addc_co_u32_e32 v93, vcc, 0, v117, vcc
	global_store_dwordx4 v[92:93], v[84:87], off offset:2048
	global_store_dwordx4 v[92:93], v[88:91], off offset:3072
	v_pk_mul_f32 v[92:93], v[76:77], v[2:3] op_sel_hi:[1,0]
	v_pk_mul_f32 v[84:85], v[68:69], v[2:3] op_sel_hi:[1,0]
	v_pk_mul_f32 v[86:87], v[70:71], v[2:3] op_sel_hi:[1,0]
	v_pk_mul_f32 v[88:89], v[72:73], v[2:3] op_sel_hi:[1,0]
	v_pk_mul_f32 v[86:87], v[26:27], v[86:87]
	v_pk_mul_f32 v[84:85], v[24:25], v[84:85]
	v_pk_mul_f32 v[88:89], v[20:21], v[88:89]
	v_pk_mul_f32 v[92:93], v[32:33], v[92:93]
	v_pk_mul_f32 v[90:91], v[74:75], v[2:3] op_sel_hi:[1,0]
	v_cvt_pk_bf16_f32 v84, v84, v85
	v_cvt_pk_bf16_f32 v85, v86, v87
	v_cvt_pk_bf16_f32 v86, v88, v89
	v_cvt_pk_bf16_f32 v88, v92, v93
	v_add_co_u32_e32 v92, vcc, 0xb000000, v114
	v_pk_mul_f32 v[90:91], v[22:23], v[90:91]
	v_pk_mul_f32 v[94:95], v[78:79], v[2:3] op_sel_hi:[1,0]
	v_pk_mul_f32 v[96:97], v[80:81], v[2:3] op_sel_hi:[1,0]
	v_pk_mul_f32 v[98:99], v[82:83], v[2:3] op_sel_hi:[1,0]
	v_cvt_pk_bf16_f32 v87, v90, v91
	v_addc_co_u32_e32 v93, vcc, 0, v115, vcc
	v_pk_mul_f32 v[94:95], v[34:35], v[94:95]
	v_pk_mul_f32 v[98:99], v[30:31], v[98:99]
	v_pk_mul_f32 v[96:97], v[28:29], v[96:97]
	v_cvt_pk_bf16_f32 v89, v94, v95
	v_cvt_pk_bf16_f32 v91, v98, v99
	s_nop 0
	v_cvt_pk_bf16_f32 v90, v96, v97
	flat_store_dwordx4 v[92:93], v[84:87] offset:2048
	flat_store_dwordx4 v[92:93], v[88:91] offset:3072

; __device__ __forceinline__ void thin_pass(const Ctx& C, const bf16* hin, bf16* hout, bf16* u, float* out, const bf16* y, const float* gpost, float cmul, const float* gpre, bool last) {
;     ...
;         for (int b = 0; b < RB; ++b) {
;             const int m = m0 + b; const v4u y0 = yr[b][0], y1 = yr[b][1], h0 = hr[b][0], h1 = hr[b][1];
;             f32x4 yv[4], h[4];
;             yv[0] = (f32x4){bf_lo(y0.x), bf_hi(y0.x), bf_lo(y0.y), bf_hi(y0.y)}; yv[1] = (f32x4){bf_lo(y0.z), bf_hi(y0.z), bf_lo(y0.w), bf_hi(y0.w)};
;             yv[2] = (f32x4){bf_lo(y1.x), bf_hi(y1.x), bf_lo(y1.y), bf_hi(y1.y)}; yv[3] = (f32x4){bf_lo(y1.z), bf_hi(y1.z), bf_lo(y1.w), bf_hi(y1.w)};
;             h[0] = (f32x4){bf_lo(h0.x), bf_hi(h0.x), bf_lo(h0.y), bf_hi(h0.y)}; h[1] = (f32x4){bf_lo(h0.z), bf_hi(h0.z), bf_lo(h0.w), bf_hi(h0.w)};
;             h[2] = (f32x4){bf_lo(h1.x), bf_hi(h1.x), bf_lo(h1.y), bf_hi(h1.y)}; h[3] = (f32x4){bf_lo(h1.z), bf_hi(h1.z), bf_lo(h1.w), bf_hi(h1.w)};
;             float ss = 0.f;
; #pragma unroll
;             for (int i = 0; i < 4; ++i) ss += (yv[i][0] * yv[i][0] + yv[i][1] * yv[i][1]) + (yv[i][2] * yv[i][2] + yv[i][3] * yv[i][3]);
;             const float ry = cmul / sqrtf(wave_sum(ss) * (1.0f / D) + RMS_EPS);
; #pragma unroll
;             for (int i = 0; i < 4; ++i) h[i] = h[i] + yv[i] * ry * g4[i];
.LBB0_742:
	s_nop 0
	v_lshlrev_b32_e32 v76, 16, v60
	v_and_b32_e32 v77, 0xffff0000, v60
	v_mul_f32_e32 v2, v76, v76
	v_lshlrev_b32_e32 v60, 16, v61
	v_pk_fma_f32 v[78:79], v[76:77], v[76:77], v[2:3] op_sel_hi:[1,1,0]
	v_and_b32_e32 v61, 0xffff0000, v61
	v_mul_f32_e32 v2, v60, v60
	v_lshlrev_b32_e32 v83, 16, v63
	v_lshlrev_b32_e32 v82, 16, v62
	v_and_b32_e32 v63, 0xffff0000, v63
	v_and_b32_e32 v62, 0xffff0000, v62
	v_lshlrev_b32_e32 v86, 16, v56
	v_lshlrev_b32_e32 v68, 16, v58
	v_pk_fma_f32 v[80:81], v[60:61], v[60:61], v[2:3] op_sel_hi:[1,1,0]
	v_pk_mul_f32 v[84:85], v[62:63], v[62:63]
	v_and_b32_e32 v87, 0xffff0000, v56
	v_mul_f32_e32 v2, v86, v86
	v_lshlrev_b32_e32 v90, 16, v57
	v_pk_fma_f32 v[84:85], v[82:83], v[82:83], v[84:85]
	v_pk_fma_f32 v[88:89], v[86:87], v[86:87], v[2:3] op_sel_hi:[1,1,0]
	v_and_b32_e32 v91, 0xffff0000, v57
	v_mul_f32_e32 v2, v90, v90
	v_mov_b32_e32 v69, v79
	v_mov_b32_e32 v92, v68
	v_mov_b32_e32 v93, v81
	v_and_b32_e32 v94, 0xffff0000, v58
	v_lshlrev_b32_e32 v70, 16, v59
	v_and_b32_e32 v71, 0xffff0000, v59
	v_pk_add_f32 v[84:85], v[84:85], v[84:85] op_sel_hi:[0,1]
	v_pk_fma_f32 v[56:57], v[90:91], v[90:91], v[2:3] op_sel_hi:[1,1,0]
	v_pk_mul_f32 v[92:93], v[68:69], v[92:93]
	v_pk_add_f32 v[78:79], v[78:79], v[80:81]
	v_mul_f32_e32 v84, v94, v94
	v_mul_f32_e32 v88, v70, v70
	v_mul_f32_e32 v56, v71, v71
	v_mov_b32_e32 v93, v79
	v_pk_add_f32 v[78:79], v[92:93], v[84:85]
	v_pk_add_f32 v[56:57], v[88:89], v[56:57]
	v_lshlrev_b32_e32 v74, 16, v52
	v_pk_add_f32 v[56:57], v[78:79], v[56:57]
	v_and_b32_e32 v75, 0xffff0000, v52
	v_add_f32_e32 v2, v56, v57
	v_lshlrev_b32_e32 v78, 16, v53
	v_and_b32_e32 v79, 0xffff0000, v53
	v_add_f32_dpp v2, v2, v2 quad_perm:[1,0,3,2] row_mask:0xf bank_mask:0xf bound_ctrl:1
	v_lshlrev_b32_e32 v80, 16, v54
	v_and_b32_e32 v81, 0xffff0000, v54
	v_add_f32_dpp v2, v2, v2 quad_perm:[2,3,0,1] row_mask:0xf bank_mask:0xf bound_ctrl:1
	v_lshlrev_b32_e32 v84, 16, v55
	v_and_b32_e32 v85, 0xffff0000, v55
	v_add_f32_dpp v2, v2, v2 row_half_mirror row_mask:0xf bank_mask:0xf bound_ctrl:1
	v_lshlrev_b32_e32 v58, 16, v64
	v_and_b32_e32 v59, 0xffff0000, v64
	v_add_f32_dpp v2, v2, v2 row_mirror row_mask:0xf bank_mask:0xf bound_ctrl:1
	v_lshlrev_b32_e32 v64, 16, v65
	v_readlane_b32 s1, v2, 16
	v_readlane_b32 s9, v2, 48
	v_readlane_b32 s4, v2, 0
	v_readlane_b32 s5, v2, 32
	v_mov_b32_e32 v56, s1
	v_mov_b32_e32 v57, s9
	v_pk_add_f32 v[56:57], s[4:5], v[56:57]
	v_and_b32_e32 v65, 0xffff0000, v65
	v_add_f32_e32 v2, v56, v57
	v_fmamk_f32 v2, v2, 0x3a800000, v214
	v_mov_b32_e32 v57, v62
	v_mov_b32_e32 v62, v83
	v_lshlrev_b32_e32 v72, 16, v66
	v_and_b32_e32 v73, 0xffff0000, v66
	v_lshlrev_b32_e32 v66, 16, v67
	v_and_b32_e32 v67, 0xffff0000, v67
	v_mov_b32_e32 v69, v94
	s_mov_b64 s[4:5], -1
	v_rsq_f32_e32 v2, v2
	s_nop 0
	v_mul_f32_e32 v2, 0.5, v2
	v_pk_mul_f32 v[52:53], v[2:3], v[76:77] op_sel_hi:[0,1]
	v_pk_mul_f32 v[54:55], v[2:3], v[60:61] op_sel_hi:[0,1]
	v_pk_fma_f32 v[52:53], v[8:9], v[52:53], v[58:59]
	v_mov_b32_e32 v56, v82
	v_pk_mul_f32 v[58:59], v[2:3], v[62:63] op_sel_hi:[0,1]
	v_pk_fma_f32 v[54:55], v[10:11], v[54:55], v[64:65]
	v_pk_mul_f32 v[56:57], v[2:3], v[56:57] op_sel_hi:[0,1]
	v_pk_fma_f32 v[58:59], v[6:7], v[58:59], v[66:67]
	v_pk_mul_f32 v[60:61], v[2:3], v[86:87] op_sel_hi:[0,1]
	v_pk_mul_f32 v[62:63], v[2:3], v[90:91] op_sel_hi:[0,1]
	v_pk_mul_f32 v[64:65], v[68:69], v[2:3] op_sel_hi:[1,0]
	v_pk_mul_f32 v[66:67], v[70:71], v[2:3] op_sel_hi:[1,0]
	v_pk_fma_f32 v[56:57], v[4:5], v[56:57], v[72:73]
	v_pk_fma_f32 v[62:63], v[18:19], v[62:63], v[78:79]
	v_pk_fma_f32 v[60:61], v[16:17], v[60:61], v[74:75]
	v_pk_fma_f32 v[66:67], v[14:15], v[66:67], v[84:85]
	v_pk_fma_f32 v[64:65], v[12:13], v[64:65], v[80:81]
	s_and_b64 vcc, exec, s[2:3]
	s_cbranch_vccnz .LBB0_744
; __device__ __forceinline__ unsigned pk2(float lo, float hi) { unsigned r; asm("v_cvt_pk_bf16_f32 %0, %1, %2" : "=v"(r) : "v"(lo), "v"(hi)); return r; }
; __device__ __forceinline__ void thin_pass(const Ctx& C, const bf16* hin, bf16* hout, bf16* u, float* out, const bf16* y, const float* gpost, float cmul, const float* gpre, bool last) {
;     ...
;                 float s2 = 0.f;
; #pragma unroll
;                 for (int i = 0; i < 4; ++i) s2 += (h[i][0] * h[i][0] + h[i][1] * h[i][1]) + (h[i][2] * h[i][2] + h[i][3] * h[i][3]);
;                 const float rh = 1.0f / sqrtf(wave_sum(s2) * (1.0f / D) + RMS_EPS);
;                 v4u o0, o1; o0.x = pk2(h[0][0], h[0][1]); o0.y = pk2(h[0][2], h[0][3]); o0.z = pk2(h[1][0], h[1][1]); o0.w = pk2(h[1][2], h[1][3]);
;                 o1.x = pk2(h[2][0], h[2][1]); o1.y = pk2(h[2][2], h[2][3]); o1.z = pk2(h[3][0], h[3][1]); o1.w = pk2(h[3][2], h[3][3]);
;                 v4u* hp = (v4u*)(hout + (size_t)m * D); hp[lane] = o0; hp[64 + lane] = o1;
; #pragma unroll
;                 for (int i = 0; i < 4; ++i) h[i] = h[i] * rh * q4[i];
;                 o0.x = pk2(h[0][0], h[0][1]); o0.y = pk2(h[0][2], h[0][3]); o0.z = pk2(h[1][0], h[1][1]); o0.w = pk2(h[1][2], h[1][3]);
;                 o1.x = pk2(h[2][0], h[2][1]); o1.y = pk2(h[2][2], h[2][3]); o1.z = pk2(h[3][0], h[3][1]); o1.w = pk2(h[3][2], h[3][3]);
;                 v4u* up = (v4u*)(u + (size_t)m * D); up[lane] = o0; up[64 + lane] = o1;
	v_pk_mul_f32 v[68:69], v[54:55], v[54:55]
	v_pk_mul_f32 v[70:71], v[52:53], v[52:53]
	v_mul_f32_e32 v2, v60, v60
	v_pk_mov_b32 v[72:73], v[70:71], v[68:69] op_sel:[1,0]
	v_mov_b32_e32 v71, v69
	v_pk_add_f32 v[68:69], v[72:73], v[70:71]
	v_pk_mul_f32 v[70:71], v[58:59], v[58:59]
	v_pk_mul_f32 v[72:73], v[56:57], v[56:57]
	v_pk_add_f32 v[68:69], v[68:69], v[68:69] op_sel_hi:[0,1]
	v_pk_mov_b32 v[74:75], v[72:73], v[70:71] op_sel:[1,0]
	v_mov_b32_e32 v73, v71
	v_pk_add_f32 v[70:71], v[74:75], v[72:73]
	v_pk_fma_f32 v[72:73], v[60:61], v[60:61], v[2:3] op_sel_hi:[1,1,0]
	v_mul_f32_e32 v2, v62, v62
	v_pk_add_f32 v[70:71], v[70:71], v[70:71] op_sel_hi:[0,1]
	v_pk_fma_f32 v[74:75], v[62:63], v[62:63], v[2:3] op_sel_hi:[1,1,0]
	v_mul_f32_e32 v72, v64, v64
	v_mul_f32_e32 v74, v65, v65
	v_mul_f32_e32 v68, v66, v66
	v_mul_f32_e32 v70, v67, v67
	v_pk_add_f32 v[72:73], v[72:73], v[74:75]
	v_pk_add_f32 v[68:69], v[68:69], v[70:71]
	v_cvt_pk_bf16_f32 v74, v64, v65
	v_cvt_pk_bf16_f32 v75, v66, v67
	s_nop 0
	v_pk_add_f32 v[68:69], v[72:73], v[68:69]
	v_cvt_pk_bf16_f32 v73, v62, v63
	s_nop 0
	v_add_f32_e32 v2, v68, v69
	s_nop 1
	v_add_f32_dpp v2, v2, v2 quad_perm:[1,0,3,2] row_mask:0xf bank_mask:0xf bound_ctrl:1
	s_nop 1
	v_add_f32_dpp v2, v2, v2 quad_perm:[2,3,0,1] row_mask:0xf bank_mask:0xf bound_ctrl:1
	s_nop 1
	v_add_f32_dpp v2, v2, v2 row_half_mirror row_mask:0xf bank_mask:0xf bound_ctrl:1
	s_nop 1
	v_add_f32_dpp v2, v2, v2 row_mirror row_mask:0xf bank_mask:0xf bound_ctrl:1
	s_nop 0
	v_readlane_b32 s1, v2, 16
	v_readlane_b32 s9, v2, 48
	v_readlane_b32 s4, v2, 0
	v_readlane_b32 s5, v2, 32
	v_mov_b32_e32 v68, s1
	v_mov_b32_e32 v69, s9
	v_pk_add_f32 v[68:69], s[4:5], v[68:69]
	s_nop 0
	v_add_f32_e32 v2, v68, v69
	v_fmamk_f32 v2, v2, 0x3a800000, v214
	s_mov_b64 s[4:5], 0
	v_add_co_u32_e32 v76, vcc, s93, v116
	v_rsq_f32_e32 v2, v2
	s_nop 0
	v_cvt_pk_bf16_f32 v68, v52, v53
	v_cvt_pk_bf16_f32 v69, v54, v55
	v_cvt_pk_bf16_f32 v70, v56, v57
	v_cvt_pk_bf16_f32 v71, v58, v59
	v_cvt_pk_bf16_f32 v72, v60, v61
	s_nop 0
	v_addc_co_u32_e32 v77, vcc, 0, v117, vcc
	global_store_dwordx4 v[76:77], v[68:71], off
	global_store_dwordx4 v[76:77], v[72:75], off offset:1024
	v_pk_mul_f32 v[76:77], v[60:61], v[2:3] op_sel_hi:[1,0]
	v_pk_mul_f32 v[68:69], v[52:53], v[2:3] op_sel_hi:[1,0]
	v_pk_mul_f32 v[70:71], v[54:55], v[2:3] op_sel_hi:[1,0]
	v_pk_mul_f32 v[72:73], v[56:57], v[2:3] op_sel_hi:[1,0]
	v_pk_mul_f32 v[70:71], v[26:27], v[70:71]
	v_pk_mul_f32 v[68:69], v[24:25], v[68:69]
	v_pk_mul_f32 v[72:73], v[20:21], v[72:73]
	v_pk_mul_f32 v[76:77], v[32:33], v[76:77]
	v_pk_mul_f32 v[74:75], v[58:59], v[2:3] op_sel_hi:[1,0]
	v_cvt_pk_bf16_f32 v68, v68, v69
	v_cvt_pk_bf16_f32 v69, v70, v71
	v_cvt_pk_bf16_f32 v70, v72, v73
	v_cvt_pk_bf16_f32 v72, v76, v77
	v_add_co_u32_e32 v76, vcc, 0xb001000, v114
	v_pk_mul_f32 v[74:75], v[22:23], v[74:75]
	v_pk_mul_f32 v[78:79], v[62:63], v[2:3] op_sel_hi:[1,0]
	v_pk_mul_f32 v[80:81], v[64:65], v[2:3] op_sel_hi:[1,0]
	v_pk_mul_f32 v[82:83], v[66:67], v[2:3] op_sel_hi:[1,0]
	v_cvt_pk_bf16_f32 v71, v74, v75
	v_addc_co_u32_e32 v77, vcc, 0, v115, vcc
	v_pk_mul_f32 v[78:79], v[34:35], v[78:79]
	v_pk_mul_f32 v[82:83], v[30:31], v[82:83]
	v_pk_mul_f32 v[80:81], v[28:29], v[80:81]
	v_cvt_pk_bf16_f32 v73, v78, v79
	v_cvt_pk_bf16_f32 v75, v82, v83
	s_nop 0
	v_cvt_pk_bf16_f32 v74, v80, v81
	flat_store_dwordx4 v[76:77], v[68:71]
	flat_store_dwordx4 v[76:77], v[72:75] offset:1024

; __device__ __forceinline__ void thin_pass(const Ctx& C, const bf16* hin, bf16* hout, bf16* u, float* out, const bf16* y, const float* gpost, float cmul, const float* gpre, bool last) {
;     ...
;         for (int b = 0; b < RB; ++b) {
;             const int m = m0 + b; const v4u y0 = yr[b][0], y1 = yr[b][1], h0 = hr[b][0], h1 = hr[b][1];
;             f32x4 yv[4], h[4];
;             yv[0] = (f32x4){bf_lo(y0.x), bf_hi(y0.x), bf_lo(y0.y), bf_hi(y0.y)}; yv[1] = (f32x4){bf_lo(y0.z), bf_hi(y0.z), bf_lo(y0.w), bf_hi(y0.w)};
;             yv[2] = (f32x4){bf_lo(y1.x), bf_hi(y1.x), bf_lo(y1.y), bf_hi(y1.y)}; yv[3] = (f32x4){bf_lo(y1.z), bf_hi(y1.z), bf_lo(y1.w), bf_hi(y1.w)};
;             h[0] = (f32x4){bf_lo(h0.x), bf_hi(h0.x), bf_lo(h0.y), bf_hi(h0.y)}; h[1] = (f32x4){bf_lo(h0.z), bf_hi(h0.z), bf_lo(h0.w), bf_hi(h0.w)};
;             h[2] = (f32x4){bf_lo(h1.x), bf_hi(h1.x), bf_lo(h1.y), bf_hi(h1.y)}; h[3] = (f32x4){bf_lo(h1.z), bf_hi(h1.z), bf_lo(h1.w), bf_hi(h1.w)};
;             float ss = 0.f;
; #pragma unroll
;             for (int i = 0; i < 4; ++i) ss += (yv[i][0] * yv[i][0] + yv[i][1] * yv[i][1]) + (yv[i][2] * yv[i][2] + yv[i][3] * yv[i][3]);
;             const float ry = cmul / sqrtf(wave_sum(ss) * (1.0f / D) + RMS_EPS);
; #pragma unroll
;             for (int i = 0; i < 4; ++i) h[i] = h[i] + yv[i] * ry * g4[i];
.LBB0_746:
	s_nop 0
	v_lshlrev_b32_e32 v60, 16, v44
	v_and_b32_e32 v61, 0xffff0000, v44
	v_mul_f32_e32 v2, v60, v60
	v_lshlrev_b32_e32 v44, 16, v45
	v_pk_fma_f32 v[62:63], v[60:61], v[60:61], v[2:3] op_sel_hi:[1,1,0]
	v_and_b32_e32 v45, 0xffff0000, v45
	v_mul_f32_e32 v2, v44, v44
	v_lshlrev_b32_e32 v67, 16, v47
	v_lshlrev_b32_e32 v66, 16, v46
	v_and_b32_e32 v47, 0xffff0000, v47
	v_and_b32_e32 v46, 0xffff0000, v46
	v_lshlrev_b32_e32 v70, 16, v40
	v_lshlrev_b32_e32 v52, 16, v42
	v_pk_fma_f32 v[64:65], v[44:45], v[44:45], v[2:3] op_sel_hi:[1,1,0]
	v_pk_mul_f32 v[68:69], v[46:47], v[46:47]
	v_and_b32_e32 v71, 0xffff0000, v40
	v_mul_f32_e32 v2, v70, v70
	v_lshlrev_b32_e32 v74, 16, v41
	v_pk_fma_f32 v[68:69], v[66:67], v[66:67], v[68:69]
	v_pk_fma_f32 v[72:73], v[70:71], v[70:71], v[2:3] op_sel_hi:[1,1,0]
	v_and_b32_e32 v75, 0xffff0000, v41
	v_mul_f32_e32 v2, v74, v74
	v_mov_b32_e32 v53, v63
	v_mov_b32_e32 v76, v52
	v_mov_b32_e32 v77, v65
	v_and_b32_e32 v78, 0xffff0000, v42
	v_lshlrev_b32_e32 v54, 16, v43
	v_and_b32_e32 v55, 0xffff0000, v43
	v_pk_add_f32 v[68:69], v[68:69], v[68:69] op_sel_hi:[0,1]
	v_pk_fma_f32 v[40:41], v[74:75], v[74:75], v[2:3] op_sel_hi:[1,1,0]
	v_pk_mul_f32 v[76:77], v[52:53], v[76:77]
	v_pk_add_f32 v[62:63], v[62:63], v[64:65]
	v_mul_f32_e32 v68, v78, v78
	v_mul_f32_e32 v72, v54, v54
	v_mul_f32_e32 v40, v55, v55
	v_mov_b32_e32 v77, v63
	v_pk_add_f32 v[62:63], v[76:77], v[68:69]
	v_pk_add_f32 v[40:41], v[72:73], v[40:41]
	v_lshlrev_b32_e32 v58, 16, v36
	v_pk_add_f32 v[40:41], v[62:63], v[40:41]
	v_and_b32_e32 v59, 0xffff0000, v36
	v_add_f32_e32 v2, v40, v41
	v_lshlrev_b32_e32 v62, 16, v37
	v_and_b32_e32 v63, 0xffff0000, v37
	v_add_f32_dpp v2, v2, v2 quad_perm:[1,0,3,2] row_mask:0xf bank_mask:0xf bound_ctrl:1
	v_lshlrev_b32_e32 v64, 16, v38
	v_and_b32_e32 v65, 0xffff0000, v38
	v_add_f32_dpp v2, v2, v2 quad_perm:[2,3,0,1] row_mask:0xf bank_mask:0xf bound_ctrl:1
	v_lshlrev_b32_e32 v68, 16, v39
	v_and_b32_e32 v69, 0xffff0000, v39
	v_add_f32_dpp v2, v2, v2 row_half_mirror row_mask:0xf bank_mask:0xf bound_ctrl:1
	v_lshlrev_b32_e32 v42, 16, v48
	v_and_b32_e32 v43, 0xffff0000, v48
	v_add_f32_dpp v2, v2, v2 row_mirror row_mask:0xf bank_mask:0xf bound_ctrl:1
	v_lshlrev_b32_e32 v48, 16, v49
	v_readlane_b32 s1, v2, 16
	v_readlane_b32 s9, v2, 48
	v_readlane_b32 s4, v2, 0
	v_readlane_b32 s5, v2, 32
	v_mov_b32_e32 v40, s1
	v_mov_b32_e32 v41, s9
	v_pk_add_f32 v[40:41], s[4:5], v[40:41]
	v_and_b32_e32 v49, 0xffff0000, v49
	v_add_f32_e32 v2, v40, v41
	v_fmamk_f32 v2, v2, 0x3a800000, v214
	v_mov_b32_e32 v41, v46
	v_mov_b32_e32 v46, v67
	v_lshlrev_b32_e32 v56, 16, v50
	v_and_b32_e32 v57, 0xffff0000, v50
	v_lshlrev_b32_e32 v50, 16, v51
	v_and_b32_e32 v51, 0xffff0000, v51
	v_mov_b32_e32 v53, v78
	v_rsq_f32_e32 v2, v2
	s_nop 0
	v_mul_f32_e32 v2, 0.5, v2
	v_pk_mul_f32 v[36:37], v[2:3], v[60:61] op_sel_hi:[0,1]
	v_pk_mul_f32 v[38:39], v[2:3], v[44:45] op_sel_hi:[0,1]
	v_pk_fma_f32 v[36:37], v[8:9], v[36:37], v[42:43]
	v_mov_b32_e32 v40, v66
	v_pk_mul_f32 v[42:43], v[2:3], v[46:47] op_sel_hi:[0,1]
	v_pk_fma_f32 v[38:39], v[10:11], v[38:39], v[48:49]
	v_pk_mul_f32 v[40:41], v[2:3], v[40:41] op_sel_hi:[0,1]
	v_pk_fma_f32 v[42:43], v[6:7], v[42:43], v[50:51]
	v_pk_mul_f32 v[44:45], v[2:3], v[70:71] op_sel_hi:[0,1]
	v_pk_mul_f32 v[46:47], v[2:3], v[74:75] op_sel_hi:[0,1]
	v_pk_mul_f32 v[48:49], v[52:53], v[2:3] op_sel_hi:[1,0]
	v_pk_mul_f32 v[50:51], v[54:55], v[2:3] op_sel_hi:[1,0]
	v_pk_fma_f32 v[40:41], v[4:5], v[40:41], v[56:57]
	v_pk_fma_f32 v[46:47], v[18:19], v[46:47], v[62:63]
	v_pk_fma_f32 v[44:45], v[16:17], v[44:45], v[58:59]
	v_pk_fma_f32 v[50:51], v[14:15], v[50:51], v[68:69]
	v_pk_fma_f32 v[48:49], v[12:13], v[48:49], v[64:65]
	s_and_b64 vcc, exec, s[2:3]
	s_mov_b64 s[2:3], -1
	s_cbranch_vccnz .LBB0_748
; __device__ __forceinline__ unsigned pk2(float lo, float hi) { unsigned r; asm("v_cvt_pk_bf16_f32 %0, %1, %2" : "=v"(r) : "v"(lo), "v"(hi)); return r; }
; __device__ __forceinline__ void thin_pass(const Ctx& C, const bf16* hin, bf16* hout, bf16* u, float* out, const bf16* y, const float* gpost, float cmul, const float* gpre, bool last) {
;     ...
;                 float s2 = 0.f;
; #pragma unroll
;                 for (int i = 0; i < 4; ++i) s2 += (h[i][0] * h[i][0] + h[i][1] * h[i][1]) + (h[i][2] * h[i][2] + h[i][3] * h[i][3]);
;                 const float rh = 1.0f / sqrtf(wave_sum(s2) * (1.0f / D) + RMS_EPS);
;                 v4u o0, o1; o0.x = pk2(h[0][0], h[0][1]); o0.y = pk2(h[0][2], h[0][3]); o0.z = pk2(h[1][0], h[1][1]); o0.w = pk2(h[1][2], h[1][3]);
;                 o1.x = pk2(h[2][0], h[2][1]); o1.y = pk2(h[2][2], h[2][3]); o1.z = pk2(h[3][0], h[3][1]); o1.w = pk2(h[3][2], h[3][3]);
;                 v4u* hp = (v4u*)(hout + (size_t)m * D); hp[lane] = o0; hp[64 + lane] = o1;
; #pragma unroll
;                 for (int i = 0; i < 4; ++i) h[i] = h[i] * rh * q4[i];
;                 o0.x = pk2(h[0][0], h[0][1]); o0.y = pk2(h[0][2], h[0][3]); o0.z = pk2(h[1][0], h[1][1]); o0.w = pk2(h[1][2], h[1][3]);
;                 o1.x = pk2(h[2][0], h[2][1]); o1.y = pk2(h[2][2], h[2][3]); o1.z = pk2(h[3][0], h[3][1]); o1.w = pk2(h[3][2], h[3][3]);
;                 v4u* up = (v4u*)(u + (size_t)m * D); up[lane] = o0; up[64 + lane] = o1;
	v_pk_mul_f32 v[52:53], v[38:39], v[38:39]
	v_pk_mul_f32 v[54:55], v[36:37], v[36:37]
	v_mul_f32_e32 v2, v44, v44
	v_pk_mov_b32 v[56:57], v[54:55], v[52:53] op_sel:[1,0]
	v_mov_b32_e32 v55, v53
	v_pk_add_f32 v[52:53], v[56:57], v[54:55]
	v_pk_mul_f32 v[54:55], v[42:43], v[42:43]
	v_pk_mul_f32 v[56:57], v[40:41], v[40:41]
	v_pk_add_f32 v[52:53], v[52:53], v[52:53] op_sel_hi:[0,1]
	v_pk_mov_b32 v[58:59], v[56:57], v[54:55] op_sel:[1,0]
	v_mov_b32_e32 v57, v55
	v_pk_add_f32 v[54:55], v[58:59], v[56:57]
	v_pk_fma_f32 v[56:57], v[44:45], v[44:45], v[2:3] op_sel_hi:[1,1,0]
	v_mul_f32_e32 v2, v46, v46
	v_pk_add_f32 v[54:55], v[54:55], v[54:55] op_sel_hi:[0,1]
	v_pk_fma_f32 v[58:59], v[46:47], v[46:47], v[2:3] op_sel_hi:[1,1,0]
	v_mul_f32_e32 v56, v48, v48
	v_mul_f32_e32 v58, v49, v49
	v_mul_f32_e32 v52, v50, v50
	v_mul_f32_e32 v54, v51, v51
	v_pk_add_f32 v[56:57], v[56:57], v[58:59]
	v_pk_add_f32 v[52:53], v[52:53], v[54:55]
	v_cvt_pk_bf16_f32 v58, v48, v49
	v_cvt_pk_bf16_f32 v59, v50, v51
	s_nop 0
	v_pk_add_f32 v[52:53], v[56:57], v[52:53]
	v_cvt_pk_bf16_f32 v57, v46, v47
	s_nop 0
	v_add_f32_e32 v2, v52, v53
	s_nop 1
	v_add_f32_dpp v2, v2, v2 quad_perm:[1,0,3,2] row_mask:0xf bank_mask:0xf bound_ctrl:1
	s_nop 1
	v_add_f32_dpp v2, v2, v2 quad_perm:[2,3,0,1] row_mask:0xf bank_mask:0xf bound_ctrl:1
	s_nop 1
	v_add_f32_dpp v2, v2, v2 row_half_mirror row_mask:0xf bank_mask:0xf bound_ctrl:1
	s_nop 1
	v_add_f32_dpp v2, v2, v2 row_mirror row_mask:0xf bank_mask:0xf bound_ctrl:1
	s_nop 0
	v_readlane_b32 s1, v2, 16
	v_readlane_b32 s4, v2, 48
	v_readlane_b32 s2, v2, 0
	v_readlane_b32 s3, v2, 32
	v_mov_b32_e32 v52, s1
	v_mov_b32_e32 v53, s4
	v_pk_add_f32 v[52:53], s[2:3], v[52:53]
	s_nop 0
	v_add_f32_e32 v2, v52, v53
	v_fmamk_f32 v2, v2, 0x3a800000, v214
	s_lshl_b64 s[2:3], s[22:23], 10
	s_lshl_b64 s[2:3], s[2:3], 1
	v_lshl_add_u64 v[60:61], v[106:107], 0, s[2:3]
	v_rsq_f32_e32 v2, v2
	s_nop 0
	v_cvt_pk_bf16_f32 v52, v36, v37
	v_cvt_pk_bf16_f32 v53, v38, v39
	v_cvt_pk_bf16_f32 v54, v40, v41
	v_cvt_pk_bf16_f32 v55, v42, v43
	v_cvt_pk_bf16_f32 v56, v44, v45
	global_store_dwordx4 v[60:61], v[52:55], off
	global_store_dwordx4 v[60:61], v[56:59], off offset:1024
	v_pk_mul_f32 v[60:61], v[44:45], v[2:3] op_sel_hi:[1,0]
	v_pk_mul_f32 v[52:53], v[36:37], v[2:3] op_sel_hi:[1,0]
	v_pk_mul_f32 v[54:55], v[38:39], v[2:3] op_sel_hi:[1,0]
	v_pk_mul_f32 v[56:57], v[40:41], v[2:3] op_sel_hi:[1,0]
	v_pk_mul_f32 v[54:55], v[26:27], v[54:55]
	v_pk_mul_f32 v[52:53], v[24:25], v[52:53]
	v_pk_mul_f32 v[58:59], v[42:43], v[2:3] op_sel_hi:[1,0]
	v_pk_mul_f32 v[56:57], v[20:21], v[56:57]
	v_pk_mul_f32 v[60:61], v[32:33], v[60:61]
	v_pk_mul_f32 v[58:59], v[22:23], v[58:59]
	v_pk_mul_f32 v[62:63], v[46:47], v[2:3] op_sel_hi:[1,0]
	v_pk_mul_f32 v[64:65], v[48:49], v[2:3] op_sel_hi:[1,0]
	v_pk_mul_f32 v[66:67], v[50:51], v[2:3] op_sel_hi:[1,0]
	v_cvt_pk_bf16_f32 v52, v52, v53
	v_cvt_pk_bf16_f32 v53, v54, v55
	v_cvt_pk_bf16_f32 v54, v56, v57
	v_cvt_pk_bf16_f32 v55, v58, v59
	v_cvt_pk_bf16_f32 v56, v60, v61
	v_lshl_add_u64 v[60:61], v[108:109], 0, s[2:3]
	s_mov_b64 s[2:3], 0
	v_pk_mul_f32 v[62:63], v[34:35], v[62:63]
	v_pk_mul_f32 v[66:67], v[30:31], v[66:67]
	v_pk_mul_f32 v[64:65], v[28:29], v[64:65]
	v_cvt_pk_bf16_f32 v57, v62, v63
	v_cvt_pk_bf16_f32 v59, v66, v67
	s_nop 0
	v_cvt_pk_bf16_f32 v58, v64, v65
	flat_store_dwordx4 v[60:61], v[52:55]
	flat_store_dwordx4 v[60:61], v[56:59] offset:1024

; __device__ __forceinline__ void thin_pass(const Ctx& C, const bf16* hin, bf16* hout, bf16* u, float* out, const bf16* y, const float* gpost, float cmul, const float* gpre, bool last) {
;     ...
;     for (int m0 = mstart; m0 < mend; m0 += mstep) {
;         v4u yr[RB][2], hr[RB][2];
; #pragma unroll
;         for (int b = 0; b < RB; ++b) { const v4u* yp = (const v4u*)(y + (size_t)(m0 + b) * D); const v4u* hp = (const v4u*)(hin + (size_t)(m0 + b) * D);
;             yr[b][0] = yp[lane]; yr[b][1] = yp[64 + lane]; hr[b][0] = hp[lane]; hr[b][1] = hp[64 + lane]; }
; #pragma unroll
;         for (int b = 0; b < RB; ++b) {
;             const int m = m0 + b; const v4u y0 = yr[b][0], y1 = yr[b][1], h0 = hr[b][0], h1 = hr[b][1];
;             f32x4 yv[4], h[4];
;             yv[0] = (f32x4){bf_lo(y0.x), bf_hi(y0.x), bf_lo(y0.y), bf_hi(y0.y)}; yv[1] = (f32x4){bf_lo(y0.z), bf_hi(y0.z), bf_lo(y0.w), bf_hi(y0.w)};
;             yv[2] = (f32x4){bf_lo(y1.x), bf_hi(y1.x), bf_lo(y1.y), bf_hi(y1.y)}; yv[3] = (f32x4){bf_lo(y1.z), bf_hi(y1.z), bf_lo(y1.w), bf_hi(y1.w)};
;             h[0] = (f32x4){bf_lo(h0.x), bf_hi(h0.x), bf_lo(h0.y), bf_hi(h0.y)}; h[1] = (f32x4){bf_lo(h0.z), bf_hi(h0.z), bf_lo(h0.w), bf_hi(h0.w)};
;             h[2] = (f32x4){bf_lo(h1.x), bf_hi(h1.x), bf_lo(h1.y), bf_hi(h1.y)}; h[3] = (f32x4){bf_lo(h1.z), bf_hi(h1.z), bf_lo(h1.w), bf_hi(h1.w)};
;             float ss = 0.f;
; #pragma unroll
;             for (int i = 0; i < 4; ++i) ss += (yv[i][0] * yv[i][0] + yv[i][1] * yv[i][1]) + (yv[i][2] * yv[i][2] + yv[i][3] * yv[i][3]);
;             const float ry = cmul / sqrtf(wave_sum(ss) * (1.0f / D) + RMS_EPS);
; #pragma unroll
;             for (int i = 0; i < 4; ++i) h[i] = h[i] + yv[i] * ry * g4[i];
;             if (last) { f32x4* op = (f32x4*)(out + (size_t)m * D); op[2 * lane] = h[0]; op[2 * lane + 1] = h[1]; op[128 + 2 * lane] = h[2]; op[128 + 2 * lane + 1] = h[3]; }
;             else {
;                 float s2 = 0.f;
; #pragma unroll
;                 for (int i = 0; i < 4; ++i) s2 += (h[i][0] * h[i][0] + h[i][1] * h[i][1]) + (h[i][2] * h[i][2] + h[i][3] * h[i][3]);
;                 const float rh = 1.0f / sqrtf(wave_sum(s2) * (1.0f / D) + RMS_EPS);
.LBB0_1757:
	v_lshl_add_u64 v[102:103], s[8:9], 0, v[92:93]
	v_add_co_u32_e32 v36, vcc, 0xd000000, v102
	v_lshl_add_u64 v[38:39], s[14:15], 0, v[92:93]
	s_nop 0
	v_addc_co_u32_e32 v37, vcc, 0, v103, vcc
	flat_load_dwordx4 v[84:87], v[36:37]
	flat_load_dwordx4 v[88:91], v[36:37] offset:1024
	v_add_co_u32_e32 v40, vcc, 0x2000000, v38
	s_add_i32 s2, s6, 3
	s_nop 0
	v_addc_co_u32_e32 v41, vcc, 0, v39, vcc
	global_load_dwordx4 v[104:107], v[40:41], off
	global_load_dwordx4 v[108:111], v[40:41], off offset:1024
	flat_load_dwordx4 v[72:75], v[36:37] offset:2048
	flat_load_dwordx4 v[68:71], v[36:37] offset:3072
	global_load_dwordx4 v[80:83], v[40:41], off offset:2048
	global_load_dwordx4 v[76:79], v[40:41], off offset:3072
	s_ashr_i32 s3, s2, 31
	v_add_co_u32_e32 v36, vcc, s91, v102
	s_lshl_b64 s[16:17], s[2:3], 11
	s_nop 0
	v_addc_co_u32_e32 v37, vcc, 0, v103, vcc
	flat_load_dwordx4 v[56:59], v[36:37]
	flat_load_dwordx4 v[52:55], v[36:37] offset:1024
	v_add_co_u32_e32 v36, vcc, s93, v38
	v_lshl_add_u64 v[44:45], v[96:97], 0, s[16:17]
	s_nop 0
	v_addc_co_u32_e32 v37, vcc, 0, v39, vcc
	global_load_dwordx4 v[64:67], v[36:37], off
	global_load_dwordx4 v[60:63], v[36:37], off offset:1024
	v_lshl_add_u64 v[36:37], v[94:95], 0, s[16:17]
	flat_load_dwordx4 v[40:43], v[36:37]
	s_nop 0
	flat_load_dwordx4 v[36:39], v[36:37] offset:1024
	s_nop 0
	global_load_dwordx4 v[48:51], v[44:45], off
	s_nop 0
	global_load_dwordx4 v[44:47], v[44:45], off offset:1024
	s_add_i32 s6, s6, s4
	s_add_u32 s8, s8, s10
	s_addc_u32 s9, s9, s11
	s_waitcnt vmcnt(0) lgkmcnt(0)
	v_lshlrev_b32_e32 v129, 16, v87
	v_lshlrev_b32_e32 v128, 16, v86
	v_lshlrev_b32_e32 v114, 16, v106
	v_and_b32_e32 v115, 0xffff0000, v106
	v_lshlrev_b32_e32 v106, 16, v84
	v_lshlrev_b32_e32 v118, 16, v107
	v_and_b32_e32 v119, 0xffff0000, v107
	v_and_b32_e32 v107, 0xffff0000, v84
	v_mul_f32_e32 v2, v106, v106
	v_lshlrev_b32_e32 v84, 16, v85
	v_lshlrev_b32_e32 v120, 16, v108
	v_and_b32_e32 v121, 0xffff0000, v108
	v_lshlrev_b32_e32 v122, 16, v109
	v_and_b32_e32 v123, 0xffff0000, v109
	v_pk_fma_f32 v[108:109], v[106:107], v[106:107], v[2:3] op_sel_hi:[1,1,0]
	v_and_b32_e32 v85, 0xffff0000, v85
	v_mul_f32_e32 v2, v84, v84
	v_and_b32_e32 v87, 0xffff0000, v87
	v_and_b32_e32 v86, 0xffff0000, v86
	v_lshlrev_b32_e32 v132, 16, v88
	v_lshlrev_b32_e32 v116, 16, v90
	v_lshlrev_b32_e32 v124, 16, v110
	v_and_b32_e32 v125, 0xffff0000, v110
	v_lshlrev_b32_e32 v126, 16, v111
	v_and_b32_e32 v127, 0xffff0000, v111
	v_pk_fma_f32 v[110:111], v[84:85], v[84:85], v[2:3] op_sel_hi:[1,1,0]
	v_pk_mul_f32 v[130:131], v[86:87], v[86:87]
	v_and_b32_e32 v133, 0xffff0000, v88
	v_mul_f32_e32 v2, v132, v132
	v_lshlrev_b32_e32 v88, 16, v89
	v_pk_fma_f32 v[130:131], v[128:129], v[128:129], v[130:131]
	v_pk_fma_f32 v[134:135], v[132:133], v[132:133], v[2:3] op_sel_hi:[1,1,0]
	v_and_b32_e32 v89, 0xffff0000, v89
	v_mul_f32_e32 v2, v88, v88
	v_mov_b32_e32 v117, v109
	v_mov_b32_e32 v138, v116
	v_mov_b32_e32 v139, v111
	v_and_b32_e32 v140, 0xffff0000, v90
	v_lshlrev_b32_e32 v90, 16, v91
	v_and_b32_e32 v91, 0xffff0000, v91
	v_pk_add_f32 v[130:131], v[130:131], v[130:131] op_sel_hi:[0,1]
	v_pk_fma_f32 v[136:137], v[88:89], v[88:89], v[2:3] op_sel_hi:[1,1,0]
	v_pk_mul_f32 v[138:139], v[116:117], v[138:139]
	v_pk_add_f32 v[108:109], v[108:109], v[110:111]
	v_mul_f32_e32 v130, v140, v140
	v_mul_f32_e32 v134, v90, v90
	v_mul_f32_e32 v136, v91, v91
	v_mov_b32_e32 v139, v109
	v_pk_add_f32 v[108:109], v[138:139], v[130:131]
	v_pk_add_f32 v[110:111], v[134:135], v[136:137]
	v_lshlrev_b32_e32 v112, 16, v104
	v_pk_add_f32 v[108:109], v[108:109], v[110:111]
	v_and_b32_e32 v113, 0xffff0000, v104
	v_add_f32_e32 v2, v108, v109
	v_lshlrev_b32_e32 v104, 16, v105
	v_and_b32_e32 v105, 0xffff0000, v105
	v_add_f32_dpp v2, v2, v2 quad_perm:[1,0,3,2] row_mask:0xf bank_mask:0xf bound_ctrl:1
	s_nop 1
	v_add_f32_dpp v2, v2, v2 quad_perm:[2,3,0,1] row_mask:0xf bank_mask:0xf bound_ctrl:1
	s_nop 1
	v_add_f32_dpp v2, v2, v2 row_half_mirror row_mask:0xf bank_mask:0xf bound_ctrl:1
	s_nop 1
	v_add_f32_dpp v2, v2, v2 row_mirror row_mask:0xf bank_mask:0xf bound_ctrl:1
	s_nop 0
	v_readlane_b32 s5, v2, 16
	v_readlane_b32 s7, v2, 48
	v_readlane_b32 s2, v2, 0
	v_readlane_b32 s3, v2, 32
	v_mov_b32_e32 v108, s5
	v_mov_b32_e32 v109, s7
	v_pk_add_f32 v[108:109], s[2:3], v[108:109]
	s_nop 0
	v_add_f32_e32 v2, v108, v109
	v_fmamk_f32 v2, v2, 0x3a800000, v214
	v_rsq_f32_e32 v2, v2
	s_nop 0
	v_pk_mul_f32 v[84:85], v[2:3], v[84:85] op_sel_hi:[0,1]
	v_pk_fma_f32 v[104:105], v[10:11], v[84:85], v[104:105]
	v_mov_b32_e32 v84, v128
	v_mov_b32_e32 v85, v86
	v_mov_b32_e32 v86, v129
	v_pk_mul_f32 v[106:107], v[2:3], v[106:107] op_sel_hi:[0,1]
	v_pk_mul_f32 v[84:85], v[2:3], v[84:85] op_sel_hi:[0,1]
	v_pk_mul_f32 v[86:87], v[2:3], v[86:87] op_sel_hi:[0,1]
	v_pk_fma_f32 v[106:107], v[8:9], v[106:107], v[112:113]
	v_pk_fma_f32 v[108:109], v[6:7], v[86:87], v[118:119]
	v_pk_fma_f32 v[112:113], v[4:5], v[84:85], v[114:115]
	v_pk_mul_f32 v[84:85], v[2:3], v[132:133] op_sel_hi:[0,1]
	v_pk_mul_f32 v[86:87], v[2:3], v[88:89] op_sel_hi:[0,1]
	v_mov_b32_e32 v117, v140
	v_pk_fma_f32 v[110:111], v[18:19], v[86:87], v[122:123]
	v_pk_fma_f32 v[114:115], v[16:17], v[84:85], v[120:121]
	v_pk_mul_f32 v[84:85], v[90:91], v[2:3] op_sel_hi:[1,0]
	v_pk_mul_f32 v[86:87], v[116:117], v[2:3] op_sel_hi:[1,0]
	v_pk_fma_f32 v[118:119], v[14:15], v[84:85], v[126:127]
	v_pk_fma_f32 v[116:117], v[12:13], v[86:87], v[124:125]
	v_pk_mul_f32 v[84:85], v[104:105], v[104:105]
	v_pk_mul_f32 v[86:87], v[106:107], v[106:107]
	v_mul_f32_e32 v2, v114, v114
	v_pk_mov_b32 v[88:89], v[86:87], v[84:85] op_sel:[1,0]
	v_mov_b32_e32 v87, v85
; __device__ __forceinline__ void thin_pass(const Ctx& C, const bf16* hin, bf16* hout, bf16* u, float* out, const bf16* y, const float* gpost, float cmul, const float* gpre, bool last) {
;     ...
;         for (int b = 0; b < RB; ++b) {
;             const int m = m0 + b; const v4u y0 = yr[b][0], y1 = yr[b][1], h0 = hr[b][0], h1 = hr[b][1];
;             f32x4 yv[4], h[4];
;             yv[0] = (f32x4){bf_lo(y0.x), bf_hi(y0.x), bf_lo(y0.y), bf_hi(y0.y)}; yv[1] = (f32x4){bf_lo(y0.z), bf_hi(y0.z), bf_lo(y0.w), bf_hi(y0.w)};
;             yv[2] = (f32x4){bf_lo(y1.x), bf_hi(y1.x), bf_lo(y1.y), bf_hi(y1.y)}; yv[3] = (f32x4){bf_lo(y1.z), bf_hi(y1.z), bf_lo(y1.w), bf_hi(y1.w)};
;             h[0] = (f32x4){bf_lo(h0.x), bf_hi(h0.x), bf_lo(h0.y), bf_hi(h0.y)}; h[1] = (f32x4){bf_lo(h0.z), bf_hi(h0.z), bf_lo(h0.w), bf_hi(h0.w)};
;             h[2] = (f32x4){bf_lo(h1.x), bf_hi(h1.x), bf_lo(h1.y), bf_hi(h1.y)}; h[3] = (f32x4){bf_lo(h1.z), bf_hi(h1.z), bf_lo(h1.w), bf_hi(h1.w)};
;             float ss = 0.f;
; #pragma unroll
;             for (int i = 0; i < 4; ++i) ss += (yv[i][0] * yv[i][0] + yv[i][1] * yv[i][1]) + (yv[i][2] * yv[i][2] + yv[i][3] * yv[i][3]);
;             const float ry = cmul / sqrtf(wave_sum(ss) * (1.0f / D) + RMS_EPS);
;     ...
;                 float s2 = 0.f;
; #pragma unroll
;                 for (int i = 0; i < 4; ++i) s2 += (h[i][0] * h[i][0] + h[i][1] * h[i][1]) + (h[i][2] * h[i][2] + h[i][3] * h[i][3]);
;                 const float rh = 1.0f / sqrtf(wave_sum(s2) * (1.0f / D) + RMS_EPS);
;                 v4u o0, o1; o0.x = pk2(h[0][0], h[0][1]); o0.y = pk2(h[0][2], h[0][3]); o0.z = pk2(h[1][0], h[1][1]); o0.w = pk2(h[1][2], h[1][3]);
;                 o1.x = pk2(h[2][0], h[2][1]); o1.y = pk2(h[2][2], h[2][3]); o1.z = pk2(h[3][0], h[3][1]); o1.w = pk2(h[3][2], h[3][3]);
;                 v4u* hp = (v4u*)(hout + (size_t)m * D); hp[lane] = o0; hp[64 + lane] = o1;
; #pragma unroll
;                 for (int i = 0; i < 4; ++i) h[i] = h[i] * rh * q4[i];
;                 o0.x = pk2(h[0][0], h[0][1]); o0.y = pk2(h[0][2], h[0][3]); o0.z = pk2(h[1][0], h[1][1]); o0.w = pk2(h[1][2], h[1][3]);
;                 o1.x = pk2(h[2][0], h[2][1]); o1.y = pk2(h[2][2], h[2][3]); o1.z = pk2(h[3][0], h[3][1]); o1.w = pk2(h[3][2], h[3][3]);
;                 v4u* up = (v4u*)(u + (size_t)m * D); up[lane] = o0; up[64 + lane] = o1;
	v_pk_add_f32 v[84:85], v[88:89], v[86:87]
	v_pk_mul_f32 v[86:87], v[108:109], v[108:109]
	v_pk_mul_f32 v[88:89], v[112:113], v[112:113]
	v_pk_add_f32 v[84:85], v[84:85], v[84:85] op_sel_hi:[0,1]
	v_pk_mov_b32 v[90:91], v[88:89], v[86:87] op_sel:[1,0]
	v_mov_b32_e32 v89, v87
	v_pk_add_f32 v[86:87], v[90:91], v[88:89]
	v_pk_fma_f32 v[88:89], v[114:115], v[114:115], v[2:3] op_sel_hi:[1,1,0]
	v_mul_f32_e32 v2, v110, v110
	v_pk_add_f32 v[86:87], v[86:87], v[86:87] op_sel_hi:[0,1]
	v_pk_fma_f32 v[90:91], v[110:111], v[110:111], v[2:3] op_sel_hi:[1,1,0]
	v_mul_f32_e32 v88, v116, v116
	v_mul_f32_e32 v90, v117, v117
	v_mul_f32_e32 v84, v118, v118
	v_mul_f32_e32 v86, v119, v119
	v_pk_add_f32 v[88:89], v[88:89], v[90:91]
	v_pk_add_f32 v[84:85], v[84:85], v[86:87]
	v_cvt_pk_bf16_f32 v90, v116, v117
	v_cvt_pk_bf16_f32 v91, v118, v119
	v_lshl_add_u64 v[120:121], s[12:13], 0, v[92:93]
	v_pk_add_f32 v[84:85], v[88:89], v[84:85]
	v_cvt_pk_bf16_f32 v89, v110, v111
	v_and_b32_e32 v128, 0xffff0000, v70
	v_add_f32_e32 v2, v84, v85
	s_add_u32 s12, s12, s10
	s_addc_u32 s13, s13, s11
	v_add_f32_dpp v2, v2, v2 quad_perm:[1,0,3,2] row_mask:0xf bank_mask:0xf bound_ctrl:1
	s_add_u32 s14, s14, s10
	s_addc_u32 s15, s15, s11
	v_add_f32_dpp v2, v2, v2 quad_perm:[2,3,0,1] row_mask:0xf bank_mask:0xf bound_ctrl:1
	s_cmp_lt_i32 s6, s1
	s_nop 0
	v_add_f32_dpp v2, v2, v2 row_half_mirror row_mask:0xf bank_mask:0xf bound_ctrl:1
	s_nop 1
	v_add_f32_dpp v2, v2, v2 row_mirror row_mask:0xf bank_mask:0xf bound_ctrl:1
	s_nop 0
	v_readlane_b32 s5, v2, 16
	v_readlane_b32 s7, v2, 48
	v_readlane_b32 s2, v2, 0
	v_readlane_b32 s3, v2, 32
	v_mov_b32_e32 v84, s5
	v_mov_b32_e32 v85, s7
	v_pk_add_f32 v[84:85], s[2:3], v[84:85]
	s_nop 0
	v_add_f32_e32 v2, v84, v85
	v_fmamk_f32 v2, v2, 0x3a800000, v214
	s_mov_b32 s2, 0xb000000
	v_rsq_f32_e32 v2, v2
	s_nop 0
	v_cvt_pk_bf16_f32 v84, v106, v107
	v_cvt_pk_bf16_f32 v85, v104, v105
	v_cvt_pk_bf16_f32 v86, v112, v113
	v_cvt_pk_bf16_f32 v87, v108, v109
	v_cvt_pk_bf16_f32 v88, v114, v115
	flat_store_dwordx4 v[120:121], v[84:87]
	flat_store_dwordx4 v[120:121], v[88:91] offset:1024
	s_nop 0
	v_pk_mul_f32 v[84:85], v[106:107], v[2:3] op_sel_hi:[1,0]
	v_pk_mul_f32 v[86:87], v[104:105], v[2:3] op_sel_hi:[1,0]
	v_pk_mul_f32 v[90:91], v[108:109], v[2:3] op_sel_hi:[1,0]
	v_pk_mul_f32 v[108:109], v[116:117], v[2:3] op_sel_hi:[1,0]
	v_pk_mul_f32 v[86:87], v[26:27], v[86:87]
	v_pk_mul_f32 v[84:85], v[24:25], v[84:85]
	v_pk_mul_f32 v[88:89], v[112:113], v[2:3] op_sel_hi:[1,0]
	v_pk_mul_f32 v[90:91], v[22:23], v[90:91]
	v_pk_mul_f32 v[104:105], v[114:115], v[2:3] op_sel_hi:[1,0]
	v_pk_mul_f32 v[108:109], v[28:29], v[108:109]
	v_pk_mul_f32 v[88:89], v[20:21], v[88:89]
	v_pk_mul_f32 v[106:107], v[110:111], v[2:3] op_sel_hi:[1,0]
	v_pk_mul_f32 v[104:105], v[32:33], v[104:105]
	v_pk_mul_f32 v[110:111], v[118:119], v[2:3] op_sel_hi:[1,0]
	v_cvt_pk_bf16_f32 v84, v84, v85
	v_cvt_pk_bf16_f32 v85, v86, v87
	v_cvt_pk_bf16_f32 v87, v90, v91
	v_cvt_pk_bf16_f32 v90, v108, v109
	v_lshlrev_b32_e32 v108, 16, v72
	v_pk_mul_f32 v[110:111], v[30:31], v[110:111]
	v_cvt_pk_bf16_f32 v86, v88, v89
	v_cvt_pk_bf16_f32 v88, v104, v105
	v_add_co_u32_e32 v104, vcc, s2, v102
	v_and_b32_e32 v109, 0xffff0000, v72
	v_mul_f32_e32 v2, v108, v108
	v_lshlrev_b32_e32 v72, 16, v73
	v_cvt_pk_bf16_f32 v91, v110, v111
	v_addc_co_u32_e32 v105, vcc, 0, v103, vcc
	v_pk_fma_f32 v[110:111], v[108:109], v[108:109], v[2:3] op_sel_hi:[1,1,0]
	v_and_b32_e32 v73, 0xffff0000, v73
	v_mul_f32_e32 v2, v72, v72
	v_lshlrev_b32_e32 v115, 16, v75
	v_lshlrev_b32_e32 v114, 16, v74
	v_and_b32_e32 v75, 0xffff0000, v75
	v_and_b32_e32 v74, 0xffff0000, v74
	v_lshlrev_b32_e32 v118, 16, v68
	v_pk_mul_f32 v[106:107], v[34:35], v[106:107]
	v_pk_fma_f32 v[112:113], v[72:73], v[72:73], v[2:3] op_sel_hi:[1,1,0]
	v_cvt_pk_bf16_f32 v89, v106, v107
	flat_store_dwordx4 v[104:105], v[84:87]
	flat_store_dwordx4 v[104:105], v[88:91] offset:1024
	v_pk_mul_f32 v[116:117], v[74:75], v[74:75]
	v_lshlrev_b32_e32 v84, 16, v70
	v_and_b32_e32 v119, 0xffff0000, v68
	v_mul_f32_e32 v2, v118, v118
	v_lshlrev_b32_e32 v68, 16, v69
	v_pk_fma_f32 v[116:117], v[114:115], v[114:115], v[116:117]
	v_pk_fma_f32 v[122:123], v[118:119], v[118:119], v[2:3] op_sel_hi:[1,1,0]
	v_and_b32_e32 v69, 0xffff0000, v69
	v_mul_f32_e32 v2, v68, v68
	v_mov_b32_e32 v85, v111
	v_mov_b32_e32 v126, v84
	v_mov_b32_e32 v127, v113
	v_lshlrev_b32_e32 v70, 16, v71
	v_and_b32_e32 v71, 0xffff0000, v71
	v_pk_add_f32 v[116:117], v[116:117], v[116:117] op_sel_hi:[0,1]
	v_pk_fma_f32 v[124:125], v[68:69], v[68:69], v[2:3] op_sel_hi:[1,1,0]
	v_pk_mul_f32 v[126:127], v[84:85], v[126:127]
	v_pk_add_f32 v[110:111], v[110:111], v[112:113]
	v_mul_f32_e32 v116, v128, v128
	v_mul_f32_e32 v122, v70, v70
	v_mul_f32_e32 v124, v71, v71
	v_mov_b32_e32 v127, v111
	v_pk_add_f32 v[110:111], v[126:127], v[116:117]
	v_pk_add_f32 v[112:113], v[122:123], v[124:125]
	v_lshlrev_b32_e32 v86, 16, v80
	v_pk_add_f32 v[110:111], v[110:111], v[112:113]
	v_and_b32_e32 v87, 0xffff0000, v80
	v_add_f32_e32 v2, v110, v111
	v_lshlrev_b32_e32 v80, 16, v81
	v_and_b32_e32 v81, 0xffff0000, v81
	v_add_f32_dpp v2, v2, v2 quad_perm:[1,0,3,2] row_mask:0xf bank_mask:0xf bound_ctrl:1
	v_lshlrev_b32_e32 v90, 16, v76
	v_and_b32_e32 v91, 0xffff0000, v76
	v_add_f32_dpp v2, v2, v2 quad_perm:[2,3,0,1] row_mask:0xf bank_mask:0xf bound_ctrl:1
	v_lshlrev_b32_e32 v76, 16, v77
	v_and_b32_e32 v77, 0xffff0000, v77
	v_add_f32_dpp v2, v2, v2 row_half_mirror row_mask:0xf bank_mask:0xf bound_ctrl:1
	v_lshlrev_b32_e32 v88, 16, v82
	v_and_b32_e32 v89, 0xffff0000, v82
	v_add_f32_dpp v2, v2, v2 row_mirror row_mask:0xf bank_mask:0xf bound_ctrl:1
; __device__ __forceinline__ void thin_pass(const Ctx& C, const bf16* hin, bf16* hout, bf16* u, float* out, const bf16* y, const float* gpost, float cmul, const float* gpre, bool last) {
;     ...
;         for (int b = 0; b < RB; ++b) {
;             const int m = m0 + b; const v4u y0 = yr[b][0], y1 = yr[b][1], h0 = hr[b][0], h1 = hr[b][1];
;             f32x4 yv[4], h[4];
;             yv[0] = (f32x4){bf_lo(y0.x), bf_hi(y0.x), bf_lo(y0.y), bf_hi(y0.y)}; yv[1] = (f32x4){bf_lo(y0.z), bf_hi(y0.z), bf_lo(y0.w), bf_hi(y0.w)};
;             yv[2] = (f32x4){bf_lo(y1.x), bf_hi(y1.x), bf_lo(y1.y), bf_hi(y1.y)}; yv[3] = (f32x4){bf_lo(y1.z), bf_hi(y1.z), bf_lo(y1.w), bf_hi(y1.w)};
;             h[0] = (f32x4){bf_lo(h0.x), bf_hi(h0.x), bf_lo(h0.y), bf_hi(h0.y)}; h[1] = (f32x4){bf_lo(h0.z), bf_hi(h0.z), bf_lo(h0.w), bf_hi(h0.w)};
;             h[2] = (f32x4){bf_lo(h1.x), bf_hi(h1.x), bf_lo(h1.y), bf_hi(h1.y)}; h[3] = (f32x4){bf_lo(h1.z), bf_hi(h1.z), bf_lo(h1.w), bf_hi(h1.w)};
;             float ss = 0.f;
; #pragma unroll
;             for (int i = 0; i < 4; ++i) ss += (yv[i][0] * yv[i][0] + yv[i][1] * yv[i][1]) + (yv[i][2] * yv[i][2] + yv[i][3] * yv[i][3]);
;             const float ry = cmul / sqrtf(wave_sum(ss) * (1.0f / D) + RMS_EPS);
; #pragma unroll
;             for (int i = 0; i < 4; ++i) h[i] = h[i] + yv[i] * ry * g4[i];
;             if (last) { f32x4* op = (f32x4*)(out + (size_t)m * D); op[2 * lane] = h[0]; op[2 * lane + 1] = h[1]; op[128 + 2 * lane] = h[2]; op[128 + 2 * lane + 1] = h[3]; }
;             else {
;                 float s2 = 0.f;
; #pragma unroll
;                 for (int i = 0; i < 4; ++i) s2 += (h[i][0] * h[i][0] + h[i][1] * h[i][1]) + (h[i][2] * h[i][2] + h[i][3] * h[i][3]);
;                 const float rh = 1.0f / sqrtf(wave_sum(s2) * (1.0f / D) + RMS_EPS);
;                 v4u o0, o1; o0.x = pk2(h[0][0], h[0][1]); o0.y = pk2(h[0][2], h[0][3]); o0.z = pk2(h[1][0], h[1][1]); o0.w = pk2(h[1][2], h[1][3]);
;                 o1.x = pk2(h[2][0], h[2][1]); o1.y = pk2(h[2][2], h[2][3]); o1.z = pk2(h[3][0], h[3][1]); o1.w = pk2(h[3][2], h[3][3]);
;                 v4u* hp = (v4u*)(hout + (size_t)m * D); hp[lane] = o0; hp[64 + lane] = o1;
; #pragma unroll
;                 for (int i = 0; i < 4; ++i) h[i] = h[i] * rh * q4[i];
	v_lshlrev_b32_e32 v106, 16, v78
	v_readlane_b32 s5, v2, 16
	v_readlane_b32 s7, v2, 48
	v_readlane_b32 s2, v2, 0
	v_readlane_b32 s3, v2, 32
	v_mov_b32_e32 v110, s5
	v_mov_b32_e32 v111, s7
	v_pk_add_f32 v[110:111], s[2:3], v[110:111]
	v_and_b32_e32 v107, 0xffff0000, v78
	v_add_f32_e32 v2, v110, v111
	v_fmamk_f32 v2, v2, 0x3a800000, v214
	v_lshlrev_b32_e32 v78, 16, v79
	v_and_b32_e32 v79, 0xffff0000, v79
	v_lshlrev_b32_e32 v82, 16, v83
	v_and_b32_e32 v83, 0xffff0000, v83
	v_rsq_f32_e32 v2, v2
	s_nop 0
	v_pk_mul_f32 v[72:73], v[2:3], v[72:73] op_sel_hi:[0,1]
	v_pk_mul_f32 v[108:109], v[2:3], v[108:109] op_sel_hi:[0,1]
	v_pk_fma_f32 v[80:81], v[10:11], v[72:73], v[80:81]
	v_mov_b32_e32 v72, v114
	v_mov_b32_e32 v73, v74
	v_pk_mul_f32 v[68:69], v[2:3], v[68:69] op_sel_hi:[0,1]
	v_mov_b32_e32 v85, v128
	v_pk_fma_f32 v[86:87], v[8:9], v[108:109], v[86:87]
	v_pk_mul_f32 v[72:73], v[2:3], v[72:73] op_sel_hi:[0,1]
	v_mov_b32_e32 v74, v115
	v_pk_fma_f32 v[76:77], v[18:19], v[68:69], v[76:77]
	v_pk_mul_f32 v[68:69], v[70:71], v[2:3] op_sel_hi:[1,0]
	v_pk_mul_f32 v[70:71], v[84:85], v[2:3] op_sel_hi:[1,0]
	v_pk_mul_f32 v[74:75], v[2:3], v[74:75] op_sel_hi:[0,1]
	v_pk_fma_f32 v[88:89], v[4:5], v[72:73], v[88:89]
	v_pk_mul_f32 v[72:73], v[2:3], v[118:119] op_sel_hi:[0,1]
	v_pk_fma_f32 v[84:85], v[12:13], v[70:71], v[106:107]
	v_pk_fma_f32 v[78:79], v[14:15], v[68:69], v[78:79]
	v_pk_mul_f32 v[68:69], v[80:81], v[80:81]
	v_pk_mul_f32 v[70:71], v[86:87], v[86:87]
	v_pk_fma_f32 v[82:83], v[6:7], v[74:75], v[82:83]
	v_pk_fma_f32 v[90:91], v[16:17], v[72:73], v[90:91]
	v_pk_mov_b32 v[72:73], v[70:71], v[68:69] op_sel:[1,0]
	v_mov_b32_e32 v71, v69
	v_pk_add_f32 v[68:69], v[72:73], v[70:71]
	v_pk_mul_f32 v[70:71], v[82:83], v[82:83]
	v_pk_mul_f32 v[72:73], v[88:89], v[88:89]
	v_mul_f32_e32 v2, v90, v90
	v_pk_mov_b32 v[74:75], v[72:73], v[70:71] op_sel:[1,0]
	v_mov_b32_e32 v73, v71
	v_pk_add_f32 v[70:71], v[74:75], v[72:73]
	v_pk_fma_f32 v[72:73], v[90:91], v[90:91], v[2:3] op_sel_hi:[1,1,0]
	v_mul_f32_e32 v2, v76, v76
	v_pk_add_f32 v[68:69], v[68:69], v[68:69] op_sel_hi:[0,1]
	v_pk_add_f32 v[70:71], v[70:71], v[70:71] op_sel_hi:[0,1]
	v_pk_fma_f32 v[74:75], v[76:77], v[76:77], v[2:3] op_sel_hi:[1,1,0]
	v_mul_f32_e32 v72, v84, v84
	v_mul_f32_e32 v74, v85, v85
	v_mul_f32_e32 v68, v78, v78
	v_mul_f32_e32 v70, v79, v79
	v_pk_add_f32 v[72:73], v[72:73], v[74:75]
	v_pk_add_f32 v[68:69], v[68:69], v[70:71]
	v_cvt_pk_bf16_f32 v74, v84, v85
	v_cvt_pk_bf16_f32 v75, v78, v79
	v_and_b32_e32 v108, 0xffff0000, v54
	v_pk_add_f32 v[68:69], v[72:73], v[68:69]
	v_cvt_pk_bf16_f32 v73, v76, v77
	s_nop 0
	v_add_f32_e32 v2, v68, v69
	s_nop 1
	v_add_f32_dpp v2, v2, v2 quad_perm:[1,0,3,2] row_mask:0xf bank_mask:0xf bound_ctrl:1
	s_nop 1
	v_add_f32_dpp v2, v2, v2 quad_perm:[2,3,0,1] row_mask:0xf bank_mask:0xf bound_ctrl:1
	s_nop 1
	v_add_f32_dpp v2, v2, v2 row_half_mirror row_mask:0xf bank_mask:0xf bound_ctrl:1
	s_nop 1
	v_add_f32_dpp v2, v2, v2 row_mirror row_mask:0xf bank_mask:0xf bound_ctrl:1
	s_nop 0
	v_readlane_b32 s5, v2, 16
	v_readlane_b32 s7, v2, 48
	v_readlane_b32 s2, v2, 0
	v_readlane_b32 s3, v2, 32
	v_mov_b32_e32 v68, s5
	v_mov_b32_e32 v69, s7
	v_pk_add_f32 v[68:69], s[2:3], v[68:69]
	s_nop 0
	v_add_f32_e32 v2, v68, v69
	v_fmamk_f32 v2, v2, 0x3a800000, v214
	v_rsq_f32_e32 v2, v2
	s_nop 0
	v_cvt_pk_bf16_f32 v68, v86, v87
	v_cvt_pk_bf16_f32 v69, v80, v81
	v_cvt_pk_bf16_f32 v70, v88, v89
	v_cvt_pk_bf16_f32 v71, v82, v83
	v_cvt_pk_bf16_f32 v72, v90, v91
	flat_store_dwordx4 v[120:121], v[68:71] offset:2048
	flat_store_dwordx4 v[120:121], v[72:75] offset:3072
	v_pk_mul_f32 v[78:79], v[78:79], v[2:3] op_sel_hi:[1,0]
	v_pk_mul_f32 v[68:69], v[86:87], v[2:3] op_sel_hi:[1,0]
	v_pk_mul_f32 v[70:71], v[80:81], v[2:3] op_sel_hi:[1,0]
	v_pk_mul_f32 v[74:75], v[82:83], v[2:3] op_sel_hi:[1,0]
	v_pk_mul_f32 v[70:71], v[26:27], v[70:71]
	v_pk_mul_f32 v[68:69], v[24:25], v[68:69]
	v_pk_mul_f32 v[74:75], v[22:23], v[74:75]
	v_pk_mul_f32 v[78:79], v[30:31], v[78:79]
	v_pk_mul_f32 v[72:73], v[88:89], v[2:3] op_sel_hi:[1,0]
	v_pk_mul_f32 v[80:81], v[90:91], v[2:3] op_sel_hi:[1,0]
	v_cvt_pk_bf16_f32 v68, v68, v69
	v_cvt_pk_bf16_f32 v69, v70, v71
	v_cvt_pk_bf16_f32 v71, v74, v75
	v_cvt_pk_bf16_f32 v75, v78, v79
	v_lshlrev_b32_e32 v78, 16, v56
	v_pk_mul_f32 v[72:73], v[20:21], v[72:73]
	v_pk_mul_f32 v[76:77], v[76:77], v[2:3] op_sel_hi:[1,0]
	v_pk_mul_f32 v[80:81], v[32:33], v[80:81]
	v_pk_mul_f32 v[82:83], v[84:85], v[2:3] op_sel_hi:[1,0]
	v_and_b32_e32 v79, 0xffff0000, v56
	v_mul_f32_e32 v2, v78, v78
	v_lshlrev_b32_e32 v56, 16, v57
	v_pk_mul_f32 v[82:83], v[28:29], v[82:83]
	v_cvt_pk_bf16_f32 v70, v72, v73
	v_cvt_pk_bf16_f32 v72, v80, v81
	v_pk_fma_f32 v[80:81], v[78:79], v[78:79], v[2:3] op_sel_hi:[1,1,0]
	v_and_b32_e32 v57, 0xffff0000, v57
	v_mul_f32_e32 v2, v56, v56
	v_lshlrev_b32_e32 v85, 16, v59
	v_lshlrev_b32_e32 v84, 16, v58
	v_and_b32_e32 v59, 0xffff0000, v59
	v_and_b32_e32 v58, 0xffff0000, v58
	v_lshlrev_b32_e32 v88, 16, v52
	v_pk_mul_f32 v[76:77], v[34:35], v[76:77]
	v_cvt_pk_bf16_f32 v74, v82, v83
	v_pk_fma_f32 v[82:83], v[56:57], v[56:57], v[2:3] op_sel_hi:[1,1,0]
	v_cvt_pk_bf16_f32 v73, v76, v77
	flat_store_dwordx4 v[104:105], v[68:71] offset:2048
	flat_store_dwordx4 v[104:105], v[72:75] offset:3072
	v_pk_mul_f32 v[86:87], v[58:59], v[58:59]
	v_lshlrev_b32_e32 v68, 16, v54
	v_and_b32_e32 v89, 0xffff0000, v52
	v_mul_f32_e32 v2, v88, v88
	v_lshlrev_b32_e32 v52, 16, v53
	v_pk_fma_f32 v[86:87], v[84:85], v[84:85], v[86:87]
	v_pk_fma_f32 v[90:91], v[88:89], v[88:89], v[2:3] op_sel_hi:[1,1,0]
	v_and_b32_e32 v53, 0xffff0000, v53
	v_mul_f32_e32 v2, v52, v52
	v_mov_b32_e32 v69, v81
; __device__ __forceinline__ void thin_pass(const Ctx& C, const bf16* hin, bf16* hout, bf16* u, float* out, const bf16* y, const float* gpost, float cmul, const float* gpre, bool last) {
;     ...
;         for (int b = 0; b < RB; ++b) {
;             const int m = m0 + b; const v4u y0 = yr[b][0], y1 = yr[b][1], h0 = hr[b][0], h1 = hr[b][1];
;             f32x4 yv[4], h[4];
;             yv[0] = (f32x4){bf_lo(y0.x), bf_hi(y0.x), bf_lo(y0.y), bf_hi(y0.y)}; yv[1] = (f32x4){bf_lo(y0.z), bf_hi(y0.z), bf_lo(y0.w), bf_hi(y0.w)};
;             yv[2] = (f32x4){bf_lo(y1.x), bf_hi(y1.x), bf_lo(y1.y), bf_hi(y1.y)}; yv[3] = (f32x4){bf_lo(y1.z), bf_hi(y1.z), bf_lo(y1.w), bf_hi(y1.w)};
;             h[0] = (f32x4){bf_lo(h0.x), bf_hi(h0.x), bf_lo(h0.y), bf_hi(h0.y)}; h[1] = (f32x4){bf_lo(h0.z), bf_hi(h0.z), bf_lo(h0.w), bf_hi(h0.w)};
;             h[2] = (f32x4){bf_lo(h1.x), bf_hi(h1.x), bf_lo(h1.y), bf_hi(h1.y)}; h[3] = (f32x4){bf_lo(h1.z), bf_hi(h1.z), bf_lo(h1.w), bf_hi(h1.w)};
;             float ss = 0.f;
; #pragma unroll
;             for (int i = 0; i < 4; ++i) ss += (yv[i][0] * yv[i][0] + yv[i][1] * yv[i][1]) + (yv[i][2] * yv[i][2] + yv[i][3] * yv[i][3]);
;             const float ry = cmul / sqrtf(wave_sum(ss) * (1.0f / D) + RMS_EPS);
; #pragma unroll
;             for (int i = 0; i < 4; ++i) h[i] = h[i] + yv[i] * ry * g4[i];
;             if (last) { f32x4* op = (f32x4*)(out + (size_t)m * D); op[2 * lane] = h[0]; op[2 * lane + 1] = h[1]; op[128 + 2 * lane] = h[2]; op[128 + 2 * lane + 1] = h[3]; }
;             else {
;                 float s2 = 0.f;
; #pragma unroll
;                 for (int i = 0; i < 4; ++i) s2 += (h[i][0] * h[i][0] + h[i][1] * h[i][1]) + (h[i][2] * h[i][2] + h[i][3] * h[i][3]);
;                 const float rh = 1.0f / sqrtf(wave_sum(s2) * (1.0f / D) + RMS_EPS);
;                 v4u o0, o1; o0.x = pk2(h[0][0], h[0][1]); o0.y = pk2(h[0][2], h[0][3]); o0.z = pk2(h[1][0], h[1][1]); o0.w = pk2(h[1][2], h[1][3]);
;                 o1.x = pk2(h[2][0], h[2][1]); o1.y = pk2(h[2][2], h[2][3]); o1.z = pk2(h[3][0], h[3][1]); o1.w = pk2(h[3][2], h[3][3]);
;                 v4u* hp = (v4u*)(hout + (size_t)m * D); hp[lane] = o0; hp[64 + lane] = o1;
; #pragma unroll
;                 for (int i = 0; i < 4; ++i) h[i] = h[i] * rh * q4[i];
	v_mov_b32_e32 v106, v68
	v_mov_b32_e32 v107, v83
	v_lshlrev_b32_e32 v54, 16, v55
	v_and_b32_e32 v55, 0xffff0000, v55
	v_pk_add_f32 v[86:87], v[86:87], v[86:87] op_sel_hi:[0,1]
	v_pk_fma_f32 v[104:105], v[52:53], v[52:53], v[2:3] op_sel_hi:[1,1,0]
	v_pk_mul_f32 v[106:107], v[68:69], v[106:107]
	v_pk_add_f32 v[80:81], v[80:81], v[82:83]
	v_mul_f32_e32 v86, v108, v108
	v_mul_f32_e32 v90, v54, v54
	v_mul_f32_e32 v104, v55, v55
	v_mov_b32_e32 v107, v81
	v_pk_add_f32 v[80:81], v[106:107], v[86:87]
	v_pk_add_f32 v[82:83], v[90:91], v[104:105]
	v_lshlrev_b32_e32 v70, 16, v64
	v_pk_add_f32 v[80:81], v[80:81], v[82:83]
	v_and_b32_e32 v71, 0xffff0000, v64
	v_add_f32_e32 v2, v80, v81
	v_lshlrev_b32_e32 v64, 16, v65
	v_and_b32_e32 v65, 0xffff0000, v65
	v_add_f32_dpp v2, v2, v2 quad_perm:[1,0,3,2] row_mask:0xf bank_mask:0xf bound_ctrl:1
	v_lshlrev_b32_e32 v74, 16, v60
	v_and_b32_e32 v75, 0xffff0000, v60
	v_add_f32_dpp v2, v2, v2 quad_perm:[2,3,0,1] row_mask:0xf bank_mask:0xf bound_ctrl:1
	v_lshlrev_b32_e32 v60, 16, v61
	v_and_b32_e32 v61, 0xffff0000, v61
	v_add_f32_dpp v2, v2, v2 row_half_mirror row_mask:0xf bank_mask:0xf bound_ctrl:1
	v_lshlrev_b32_e32 v72, 16, v66
	v_and_b32_e32 v73, 0xffff0000, v66
	v_add_f32_dpp v2, v2, v2 row_mirror row_mask:0xf bank_mask:0xf bound_ctrl:1
	v_lshlrev_b32_e32 v76, 16, v62
	v_readlane_b32 s5, v2, 16
	v_readlane_b32 s7, v2, 48
	v_readlane_b32 s2, v2, 0
	v_readlane_b32 s3, v2, 32
	v_mov_b32_e32 v80, s5
	v_mov_b32_e32 v81, s7
	v_pk_add_f32 v[80:81], s[2:3], v[80:81]
	v_and_b32_e32 v77, 0xffff0000, v62
	v_add_f32_e32 v2, v80, v81
	v_fmamk_f32 v2, v2, 0x3a800000, v214
	v_lshlrev_b32_e32 v62, 16, v63
	v_and_b32_e32 v63, 0xffff0000, v63
	v_lshlrev_b32_e32 v66, 16, v67
	v_and_b32_e32 v67, 0xffff0000, v67
	v_rsq_f32_e32 v2, v2
	s_nop 0
	v_pk_mul_f32 v[56:57], v[2:3], v[56:57] op_sel_hi:[0,1]
	v_pk_mul_f32 v[78:79], v[2:3], v[78:79] op_sel_hi:[0,1]
	v_pk_fma_f32 v[64:65], v[10:11], v[56:57], v[64:65]
	v_mov_b32_e32 v56, v84
	v_mov_b32_e32 v57, v58
	v_pk_mul_f32 v[52:53], v[2:3], v[52:53] op_sel_hi:[0,1]
	v_mov_b32_e32 v69, v108
	v_pk_fma_f32 v[70:71], v[8:9], v[78:79], v[70:71]
	v_pk_mul_f32 v[56:57], v[2:3], v[56:57] op_sel_hi:[0,1]
	v_mov_b32_e32 v58, v85
	v_pk_fma_f32 v[60:61], v[18:19], v[52:53], v[60:61]
	v_pk_mul_f32 v[52:53], v[54:55], v[2:3] op_sel_hi:[1,0]
	v_pk_mul_f32 v[54:55], v[68:69], v[2:3] op_sel_hi:[1,0]
	v_pk_mul_f32 v[58:59], v[2:3], v[58:59] op_sel_hi:[0,1]
	v_pk_fma_f32 v[72:73], v[4:5], v[56:57], v[72:73]
	v_pk_mul_f32 v[56:57], v[2:3], v[88:89] op_sel_hi:[0,1]
	v_pk_fma_f32 v[68:69], v[12:13], v[54:55], v[76:77]
	v_pk_fma_f32 v[62:63], v[14:15], v[52:53], v[62:63]
	v_pk_mul_f32 v[52:53], v[64:65], v[64:65]
	v_pk_mul_f32 v[54:55], v[70:71], v[70:71]
	v_pk_fma_f32 v[66:67], v[6:7], v[58:59], v[66:67]
	v_pk_fma_f32 v[74:75], v[16:17], v[56:57], v[74:75]
	v_pk_mov_b32 v[56:57], v[54:55], v[52:53] op_sel:[1,0]
	v_mov_b32_e32 v55, v53
	v_pk_add_f32 v[52:53], v[56:57], v[54:55]
	v_pk_mul_f32 v[54:55], v[66:67], v[66:67]
	v_pk_mul_f32 v[56:57], v[72:73], v[72:73]
	v_mul_f32_e32 v2, v74, v74
	v_pk_mov_b32 v[58:59], v[56:57], v[54:55] op_sel:[1,0]
	v_mov_b32_e32 v57, v55
	v_pk_add_f32 v[54:55], v[58:59], v[56:57]
	v_pk_fma_f32 v[56:57], v[74:75], v[74:75], v[2:3] op_sel_hi:[1,1,0]
	v_mul_f32_e32 v2, v60, v60
	v_pk_add_f32 v[52:53], v[52:53], v[52:53] op_sel_hi:[0,1]
	v_pk_add_f32 v[54:55], v[54:55], v[54:55] op_sel_hi:[0,1]
	v_pk_fma_f32 v[58:59], v[60:61], v[60:61], v[2:3] op_sel_hi:[1,1,0]
	v_mul_f32_e32 v56, v68, v68
	v_mul_f32_e32 v58, v69, v69
	v_mul_f32_e32 v52, v62, v62
	v_mul_f32_e32 v54, v63, v63
	v_pk_add_f32 v[56:57], v[56:57], v[58:59]
	v_pk_add_f32 v[52:53], v[52:53], v[54:55]
	v_cvt_pk_bf16_f32 v58, v68, v69
	v_cvt_pk_bf16_f32 v59, v62, v63
	v_and_b32_e32 v80, 0xffff0000, v38
	v_pk_add_f32 v[52:53], v[56:57], v[52:53]
	v_cvt_pk_bf16_f32 v57, v60, v61
	s_nop 0
	v_add_f32_e32 v2, v52, v53
	s_nop 1
	v_add_f32_dpp v2, v2, v2 quad_perm:[1,0,3,2] row_mask:0xf bank_mask:0xf bound_ctrl:1
	s_nop 1
	v_add_f32_dpp v2, v2, v2 quad_perm:[2,3,0,1] row_mask:0xf bank_mask:0xf bound_ctrl:1
	s_nop 1
	v_add_f32_dpp v2, v2, v2 row_half_mirror row_mask:0xf bank_mask:0xf bound_ctrl:1
	s_nop 1
	v_add_f32_dpp v2, v2, v2 row_mirror row_mask:0xf bank_mask:0xf bound_ctrl:1
	s_nop 0
	v_readlane_b32 s5, v2, 16
	v_readlane_b32 s7, v2, 48
	v_readlane_b32 s2, v2, 0
	v_readlane_b32 s3, v2, 32
	v_mov_b32_e32 v52, s5
	v_mov_b32_e32 v53, s7
	v_pk_add_f32 v[52:53], s[2:3], v[52:53]
	s_nop 0
	v_add_f32_e32 v2, v52, v53
	v_fmamk_f32 v2, v2, 0x3a800000, v214
	s_mov_b32 s2, 0xb001000
	v_add_co_u32_e32 v76, vcc, s84, v120
	v_rsq_f32_e32 v2, v2
	s_nop 0
	v_cvt_pk_bf16_f32 v52, v70, v71
	v_cvt_pk_bf16_f32 v53, v64, v65
	v_cvt_pk_bf16_f32 v54, v72, v73
	v_cvt_pk_bf16_f32 v55, v66, v67
	s_nop 0
	v_addc_co_u32_e32 v77, vcc, 0, v121, vcc
	v_cvt_pk_bf16_f32 v56, v74, v75
	flat_store_dwordx4 v[76:77], v[52:55]
	flat_store_dwordx4 v[76:77], v[56:59] offset:1024
	v_pk_mul_f32 v[62:63], v[62:63], v[2:3] op_sel_hi:[1,0]
	v_pk_mul_f32 v[52:53], v[70:71], v[2:3] op_sel_hi:[1,0]
	v_pk_mul_f32 v[54:55], v[64:65], v[2:3] op_sel_hi:[1,0]
	v_pk_mul_f32 v[58:59], v[66:67], v[2:3] op_sel_hi:[1,0]
	v_pk_mul_f32 v[54:55], v[26:27], v[54:55]
	v_pk_mul_f32 v[52:53], v[24:25], v[52:53]
	v_pk_mul_f32 v[56:57], v[72:73], v[2:3] op_sel_hi:[1,0]
	v_pk_mul_f32 v[58:59], v[22:23], v[58:59]
	v_pk_mul_f32 v[60:61], v[60:61], v[2:3] op_sel_hi:[1,0]
	v_pk_mul_f32 v[62:63], v[30:31], v[62:63]
	v_pk_mul_f32 v[56:57], v[20:21], v[56:57]
	v_pk_mul_f32 v[64:65], v[74:75], v[2:3] op_sel_hi:[1,0]
	v_pk_mul_f32 v[60:61], v[34:35], v[60:61]
	v_cvt_pk_bf16_f32 v52, v52, v53
; __device__ __forceinline__ void thin_pass(const Ctx& C, const bf16* hin, bf16* hout, bf16* u, float* out, const bf16* y, const float* gpost, float cmul, const float* gpre, bool last) {
;     ...
;         for (int b = 0; b < RB; ++b) {
;             const int m = m0 + b; const v4u y0 = yr[b][0], y1 = yr[b][1], h0 = hr[b][0], h1 = hr[b][1];
;             f32x4 yv[4], h[4];
;             yv[0] = (f32x4){bf_lo(y0.x), bf_hi(y0.x), bf_lo(y0.y), bf_hi(y0.y)}; yv[1] = (f32x4){bf_lo(y0.z), bf_hi(y0.z), bf_lo(y0.w), bf_hi(y0.w)};
;             yv[2] = (f32x4){bf_lo(y1.x), bf_hi(y1.x), bf_lo(y1.y), bf_hi(y1.y)}; yv[3] = (f32x4){bf_lo(y1.z), bf_hi(y1.z), bf_lo(y1.w), bf_hi(y1.w)};
;             h[0] = (f32x4){bf_lo(h0.x), bf_hi(h0.x), bf_lo(h0.y), bf_hi(h0.y)}; h[1] = (f32x4){bf_lo(h0.z), bf_hi(h0.z), bf_lo(h0.w), bf_hi(h0.w)};
;             h[2] = (f32x4){bf_lo(h1.x), bf_hi(h1.x), bf_lo(h1.y), bf_hi(h1.y)}; h[3] = (f32x4){bf_lo(h1.z), bf_hi(h1.z), bf_lo(h1.w), bf_hi(h1.w)};
;             float ss = 0.f;
; #pragma unroll
;             for (int i = 0; i < 4; ++i) ss += (yv[i][0] * yv[i][0] + yv[i][1] * yv[i][1]) + (yv[i][2] * yv[i][2] + yv[i][3] * yv[i][3]);
;             const float ry = cmul / sqrtf(wave_sum(ss) * (1.0f / D) + RMS_EPS);
; #pragma unroll
;             for (int i = 0; i < 4; ++i) h[i] = h[i] + yv[i] * ry * g4[i];
	v_cvt_pk_bf16_f32 v53, v54, v55
	v_cvt_pk_bf16_f32 v55, v58, v59
	v_cvt_pk_bf16_f32 v59, v62, v63
	v_lshlrev_b32_e32 v62, 16, v40
	v_pk_mul_f32 v[64:65], v[32:33], v[64:65]
	v_pk_mul_f32 v[66:67], v[68:69], v[2:3] op_sel_hi:[1,0]
	v_cvt_pk_bf16_f32 v54, v56, v57
	v_cvt_pk_bf16_f32 v57, v60, v61
	v_add_co_u32_e32 v60, vcc, s2, v102
	v_and_b32_e32 v63, 0xffff0000, v40
	v_mul_f32_e32 v2, v62, v62
	v_lshlrev_b32_e32 v40, 16, v41
	v_pk_mul_f32 v[66:67], v[28:29], v[66:67]
	v_cvt_pk_bf16_f32 v56, v64, v65
	v_addc_co_u32_e32 v61, vcc, 0, v103, vcc
	v_pk_fma_f32 v[64:65], v[62:63], v[62:63], v[2:3] op_sel_hi:[1,1,0]
	v_and_b32_e32 v41, 0xffff0000, v41
	v_mul_f32_e32 v2, v40, v40
	v_lshlrev_b32_e32 v69, 16, v43
	v_lshlrev_b32_e32 v68, 16, v42
	v_and_b32_e32 v43, 0xffff0000, v43
	v_and_b32_e32 v42, 0xffff0000, v42
	v_lshlrev_b32_e32 v72, 16, v36
	v_cvt_pk_bf16_f32 v58, v66, v67
	flat_store_dwordx4 v[60:61], v[52:55]
	flat_store_dwordx4 v[60:61], v[56:59] offset:1024
	v_pk_fma_f32 v[66:67], v[40:41], v[40:41], v[2:3] op_sel_hi:[1,1,0]
	v_lshlrev_b32_e32 v52, 16, v38
	v_pk_mul_f32 v[70:71], v[42:43], v[42:43]
	v_and_b32_e32 v73, 0xffff0000, v36
	v_mul_f32_e32 v2, v72, v72
	v_lshlrev_b32_e32 v36, 16, v37
	v_pk_fma_f32 v[70:71], v[68:69], v[68:69], v[70:71]
	v_pk_fma_f32 v[74:75], v[72:73], v[72:73], v[2:3] op_sel_hi:[1,1,0]
	v_and_b32_e32 v37, 0xffff0000, v37
	v_mul_f32_e32 v2, v36, v36
	v_mov_b32_e32 v53, v65
	v_mov_b32_e32 v78, v52
	v_mov_b32_e32 v79, v67
	v_lshlrev_b32_e32 v38, 16, v39
	v_and_b32_e32 v39, 0xffff0000, v39
	v_pk_add_f32 v[70:71], v[70:71], v[70:71] op_sel_hi:[0,1]
	v_pk_fma_f32 v[76:77], v[36:37], v[36:37], v[2:3] op_sel_hi:[1,1,0]
	v_pk_mul_f32 v[78:79], v[52:53], v[78:79]
	v_pk_add_f32 v[64:65], v[64:65], v[66:67]
	v_mul_f32_e32 v70, v80, v80
	v_mul_f32_e32 v74, v38, v38
	v_mul_f32_e32 v76, v39, v39
	v_mov_b32_e32 v79, v65
	v_pk_add_f32 v[64:65], v[78:79], v[70:71]
	v_pk_add_f32 v[66:67], v[74:75], v[76:77]
	v_lshlrev_b32_e32 v54, 16, v48
	v_pk_add_f32 v[64:65], v[64:65], v[66:67]
	v_and_b32_e32 v55, 0xffff0000, v48
	v_add_f32_e32 v2, v64, v65
	v_lshlrev_b32_e32 v48, 16, v49
	v_and_b32_e32 v49, 0xffff0000, v49
	v_add_f32_dpp v2, v2, v2 quad_perm:[1,0,3,2] row_mask:0xf bank_mask:0xf bound_ctrl:1
	v_lshlrev_b32_e32 v58, 16, v44
	v_and_b32_e32 v59, 0xffff0000, v44
	v_add_f32_dpp v2, v2, v2 quad_perm:[2,3,0,1] row_mask:0xf bank_mask:0xf bound_ctrl:1
	v_lshlrev_b32_e32 v44, 16, v45
	v_and_b32_e32 v45, 0xffff0000, v45
	v_add_f32_dpp v2, v2, v2 row_half_mirror row_mask:0xf bank_mask:0xf bound_ctrl:1
	v_lshlrev_b32_e32 v56, 16, v50
	v_and_b32_e32 v57, 0xffff0000, v50
	v_add_f32_dpp v2, v2, v2 row_mirror row_mask:0xf bank_mask:0xf bound_ctrl:1
	v_lshlrev_b32_e32 v50, 16, v51
	v_readlane_b32 s5, v2, 16
	v_readlane_b32 s7, v2, 48
	v_readlane_b32 s2, v2, 0
	v_readlane_b32 s3, v2, 32
	v_mov_b32_e32 v64, s5
	v_mov_b32_e32 v65, s7
	v_pk_add_f32 v[64:65], s[2:3], v[64:65]
	v_and_b32_e32 v51, 0xffff0000, v51
	v_add_f32_e32 v2, v64, v65
	v_fmamk_f32 v2, v2, 0x3a800000, v214
	v_lshlrev_b32_e32 v60, 16, v46
	v_and_b32_e32 v61, 0xffff0000, v46
	v_lshlrev_b32_e32 v46, 16, v47
	v_and_b32_e32 v47, 0xffff0000, v47
	v_rsq_f32_e32 v2, v2
	s_nop 0
	v_pk_mul_f32 v[40:41], v[2:3], v[40:41] op_sel_hi:[0,1]
	v_pk_mul_f32 v[62:63], v[2:3], v[62:63] op_sel_hi:[0,1]
	v_pk_fma_f32 v[48:49], v[10:11], v[40:41], v[48:49]
	v_mov_b32_e32 v40, v69
	v_mov_b32_e32 v41, v43
	v_pk_mul_f32 v[36:37], v[2:3], v[36:37] op_sel_hi:[0,1]
	v_mov_b32_e32 v53, v80
	v_pk_fma_f32 v[54:55], v[8:9], v[62:63], v[54:55]
	v_pk_mul_f32 v[40:41], v[2:3], v[40:41] op_sel_hi:[0,1]
	v_mov_b32_e32 v69, v42
	v_pk_fma_f32 v[44:45], v[18:19], v[36:37], v[44:45]
	v_pk_mul_f32 v[36:37], v[38:39], v[2:3] op_sel_hi:[1,0]
; __device__ __forceinline__ unsigned pk2(float lo, float hi) { unsigned r; asm("v_cvt_pk_bf16_f32 %0, %1, %2" : "=v"(r) : "v"(lo), "v"(hi)); return r; }
; __device__ __forceinline__ void thin_pass(const Ctx& C, const bf16* hin, bf16* hout, bf16* u, float* out, const bf16* y, const float* gpost, float cmul, const float* gpre, bool last) {
;     ...
;                 float s2 = 0.f;
; #pragma unroll
;                 for (int i = 0; i < 4; ++i) s2 += (h[i][0] * h[i][0] + h[i][1] * h[i][1]) + (h[i][2] * h[i][2] + h[i][3] * h[i][3]);
;                 const float rh = 1.0f / sqrtf(wave_sum(s2) * (1.0f / D) + RMS_EPS);
;                 v4u o0, o1; o0.x = pk2(h[0][0], h[0][1]); o0.y = pk2(h[0][2], h[0][3]); o0.z = pk2(h[1][0], h[1][1]); o0.w = pk2(h[1][2], h[1][3]);
;                 o1.x = pk2(h[2][0], h[2][1]); o1.y = pk2(h[2][2], h[2][3]); o1.z = pk2(h[3][0], h[3][1]); o1.w = pk2(h[3][2], h[3][3]);
;                 v4u* hp = (v4u*)(hout + (size_t)m * D); hp[lane] = o0; hp[64 + lane] = o1;
; #pragma unroll
;                 for (int i = 0; i < 4; ++i) h[i] = h[i] * rh * q4[i];
;                 o0.x = pk2(h[0][0], h[0][1]); o0.y = pk2(h[0][2], h[0][3]); o0.z = pk2(h[1][0], h[1][1]); o0.w = pk2(h[1][2], h[1][3]);
;                 o1.x = pk2(h[2][0], h[2][1]); o1.y = pk2(h[2][2], h[2][3]); o1.z = pk2(h[3][0], h[3][1]); o1.w = pk2(h[3][2], h[3][3]);
;                 v4u* up = (v4u*)(u + (size_t)m * D); up[lane] = o0; up[64 + lane] = o1;
	v_pk_mul_f32 v[38:39], v[52:53], v[2:3] op_sel_hi:[1,0]
	v_pk_mul_f32 v[42:43], v[2:3], v[68:69] op_sel_hi:[0,1]
	v_pk_fma_f32 v[50:51], v[6:7], v[40:41], v[50:51]
	v_pk_mul_f32 v[40:41], v[2:3], v[72:73] op_sel_hi:[0,1]
	v_pk_fma_f32 v[52:53], v[12:13], v[38:39], v[60:61]
	v_pk_fma_f32 v[46:47], v[14:15], v[36:37], v[46:47]
	v_pk_mul_f32 v[36:37], v[48:49], v[48:49]
	v_pk_mul_f32 v[38:39], v[54:55], v[54:55]
	v_pk_fma_f32 v[56:57], v[4:5], v[42:43], v[56:57]
	v_pk_fma_f32 v[58:59], v[16:17], v[40:41], v[58:59]
	v_pk_mov_b32 v[40:41], v[38:39], v[36:37] op_sel:[1,0]
	v_mov_b32_e32 v39, v37
	v_pk_add_f32 v[36:37], v[40:41], v[38:39]
	v_pk_mul_f32 v[38:39], v[50:51], v[50:51]
	v_pk_mul_f32 v[40:41], v[56:57], v[56:57]
	v_mul_f32_e32 v2, v58, v58
	v_pk_mov_b32 v[42:43], v[40:41], v[38:39] op_sel:[1,0]
	v_mov_b32_e32 v41, v39
	v_pk_add_f32 v[38:39], v[42:43], v[40:41]
	v_pk_fma_f32 v[40:41], v[58:59], v[58:59], v[2:3] op_sel_hi:[1,1,0]
	v_mul_f32_e32 v2, v44, v44
	v_pk_add_f32 v[36:37], v[36:37], v[36:37] op_sel_hi:[0,1]
	v_pk_add_f32 v[38:39], v[38:39], v[38:39] op_sel_hi:[0,1]
	v_pk_fma_f32 v[42:43], v[44:45], v[44:45], v[2:3] op_sel_hi:[1,1,0]
	v_mul_f32_e32 v40, v52, v52
	v_mul_f32_e32 v42, v53, v53
	v_mul_f32_e32 v36, v46, v46
	v_mul_f32_e32 v38, v47, v47
	v_pk_add_f32 v[40:41], v[40:41], v[42:43]
	v_pk_add_f32 v[36:37], v[36:37], v[38:39]
	v_lshl_add_u64 v[60:61], v[98:99], 0, s[16:17]
	v_pk_add_f32 v[36:37], v[40:41], v[36:37]
	v_cvt_pk_bf16_f32 v41, v44, v45
	v_cvt_pk_bf16_f32 v42, v52, v53
	v_cvt_pk_bf16_f32 v43, v46, v47
	s_nop 0
	v_add_f32_e32 v2, v36, v37
	s_nop 1
	v_add_f32_dpp v2, v2, v2 quad_perm:[1,0,3,2] row_mask:0xf bank_mask:0xf bound_ctrl:1
	s_nop 1
	v_add_f32_dpp v2, v2, v2 quad_perm:[2,3,0,1] row_mask:0xf bank_mask:0xf bound_ctrl:1
	s_nop 1
	v_add_f32_dpp v2, v2, v2 row_half_mirror row_mask:0xf bank_mask:0xf bound_ctrl:1
	s_nop 1
	v_add_f32_dpp v2, v2, v2 row_mirror row_mask:0xf bank_mask:0xf bound_ctrl:1
	s_nop 0
	v_readlane_b32 s5, v2, 16
	v_readlane_b32 s7, v2, 48
	v_readlane_b32 s2, v2, 0
	v_readlane_b32 s3, v2, 32
	v_mov_b32_e32 v36, s5
	v_mov_b32_e32 v37, s7
	v_pk_add_f32 v[36:37], s[2:3], v[36:37]
	s_nop 0
	v_add_f32_e32 v2, v36, v37
	v_fmamk_f32 v2, v2, 0x3a800000, v214
	v_rsq_f32_e32 v2, v2
	s_nop 0
	v_cvt_pk_bf16_f32 v36, v54, v55
	v_cvt_pk_bf16_f32 v37, v48, v49
	v_cvt_pk_bf16_f32 v38, v56, v57
	v_cvt_pk_bf16_f32 v39, v50, v51
	v_cvt_pk_bf16_f32 v40, v58, v59
	flat_store_dwordx4 v[60:61], v[36:39]
	flat_store_dwordx4 v[60:61], v[40:43] offset:1024
	v_pk_mul_f32 v[44:45], v[44:45], v[2:3] op_sel_hi:[1,0]
	v_pk_mul_f32 v[36:37], v[54:55], v[2:3] op_sel_hi:[1,0]
	v_pk_mul_f32 v[38:39], v[48:49], v[2:3] op_sel_hi:[1,0]
	v_pk_mul_f32 v[40:41], v[56:57], v[2:3] op_sel_hi:[1,0]
	v_pk_mul_f32 v[38:39], v[26:27], v[38:39]
	v_pk_mul_f32 v[36:37], v[24:25], v[36:37]
	v_pk_mul_f32 v[42:43], v[50:51], v[2:3] op_sel_hi:[1,0]
	v_pk_mul_f32 v[40:41], v[20:21], v[40:41]
	v_pk_mul_f32 v[44:45], v[34:35], v[44:45]
	v_pk_mul_f32 v[42:43], v[22:23], v[42:43]
	v_pk_mul_f32 v[48:49], v[58:59], v[2:3] op_sel_hi:[1,0]
	v_pk_mul_f32 v[50:51], v[52:53], v[2:3] op_sel_hi:[1,0]
	v_pk_mul_f32 v[46:47], v[46:47], v[2:3] op_sel_hi:[1,0]
	v_cvt_pk_bf16_f32 v36, v36, v37
	v_cvt_pk_bf16_f32 v37, v38, v39
	v_cvt_pk_bf16_f32 v38, v40, v41
	v_cvt_pk_bf16_f32 v39, v42, v43
	v_cvt_pk_bf16_f32 v41, v44, v45
	v_lshl_add_u64 v[44:45], v[100:101], 0, s[16:17]
	v_pk_mul_f32 v[48:49], v[32:33], v[48:49]
	v_pk_mul_f32 v[46:47], v[30:31], v[46:47]
	v_pk_mul_f32 v[50:51], v[28:29], v[50:51]
	v_cvt_pk_bf16_f32 v40, v48, v49
	v_cvt_pk_bf16_f32 v43, v46, v47
	s_nop 0
	v_cvt_pk_bf16_f32 v42, v50, v51
	flat_store_dwordx4 v[44:45], v[36:39]
	flat_store_dwordx4 v[44:45], v[40:43] offset:1024
	s_cbranch_scc1 .LBB0_1757
